# softshrink as a - med3(a,-l,l): no compares/selects, ~60 fewer instructions before the second barrier
# baseline (speedup 1.0000x reference)
_Z12fused_kernelPKfS0_Pf:
	s_load_dwordx4 s[12:15], s[0:1], 0x0
	s_load_dwordx2 s[8:9], s[0:1], 0x10
	s_lshl_b32 s0, s2, 5
	s_and_b32 s0, s0, 0xe0
	s_lshr_b32 s3, s2, 3
	s_add_i32 s0, s0, s3
	v_and_b32_e32 v1, 63, v0
	v_lshrrev_b32_e32 v200, 6, v0
	s_lshl_b32 s0, s0, 17
	v_lshlrev_b32_e32 v194, 4, v0
	v_lshl_add_u32 v2, v200, 25, s0
	v_lshlrev_b32_e32 v198, 4, v1
	v_add_u32_e32 v106, 0x2000, v194
	v_add_u32_e32 v107, 0x4000, v194
	v_or_b32_e32 v203, v2, v198
	v_lshlrev_b32_e32 v196, 10, v200
	v_mov_b32_e32 v195, 0
	v_or_b32_e32 v233, v203, v196
	s_mov_b32 s7, 0x20000
	s_brev_b32 s6, 8
	s_waitcnt lgkmcnt(0)
	s_and_b32 s5, s13, 0xffff
	s_mov_b32 s4, s12
	buffer_load_dwordx4 v[70:73], v233, s[4:7], 0 offen nt
	v_or_b32_e32 v227, 0x2000, v233
	buffer_load_dwordx4 v[66:69], v227, s[4:7], 0 offen nt
	v_or_b32_e32 v226, 0x4000, v233
	buffer_load_dwordx4 v[78:81], v226, s[4:7], 0 offen nt
	v_or_b32_e32 v227, 0x6000, v233
	buffer_load_dwordx4 v[74:77], v227, s[4:7], 0 offen nt
	v_or_b32_e32 v226, 0x8000, v233
	buffer_load_dwordx4 v[86:89], v226, s[4:7], 0 offen nt
	v_or_b32_e32 v227, 0xa000, v233
	buffer_load_dwordx4 v[82:85], v227, s[4:7], 0 offen nt
	v_or_b32_e32 v226, 0xc000, v233
	buffer_load_dwordx4 v[94:97], v226, s[4:7], 0 offen nt
	v_or_b32_e32 v227, 0xe000, v233
	buffer_load_dwordx4 v[90:93], v227, s[4:7], 0 offen nt
	v_or_b32_e32 v226, 0x10000, v233
	buffer_load_dwordx4 v[150:153], v226, s[4:7], 0 offen nt
	v_or_b32_e32 v227, 0x12000, v233
	buffer_load_dwordx4 v[146:149], v227, s[4:7], 0 offen nt
	v_or_b32_e32 v226, 0x14000, v233
	buffer_load_dwordx4 v[162:165], v226, s[4:7], 0 offen nt
	v_or_b32_e32 v227, 0x16000, v233
	buffer_load_dwordx4 v[154:157], v227, s[4:7], 0 offen nt
	v_or_b32_e32 v226, 0x18000, v233
	buffer_load_dwordx4 v[174:177], v226, s[4:7], 0 offen nt
	v_or_b32_e32 v227, 0x1a000, v233
	buffer_load_dwordx4 v[166:169], v227, s[4:7], 0 offen nt
	v_or_b32_e32 v226, 0x1c000, v233
	buffer_load_dwordx4 v[182:185], v226, s[4:7], 0 offen nt
	v_or_b32_e32 v227, 0x1e000, v233
	buffer_load_dwordx4 v[178:181], v227, s[4:7], 0 offen nt
	global_load_dwordx4 v[228:231], v194, s[14:15]
	global_load_dwordx4 v[98:101], v106, s[14:15]
	global_load_dwordx4 v[102:105], v107, s[14:15]
	v_add_u32_e32 v107, 0x6000, v194
	global_load_dwordx4 v[116:119], v107, s[14:15]
	v_add_u32_e32 v106, 0x8000, v194
	global_load_dwordx4 v[120:123], v106, s[14:15]
	v_add_u32_e32 v107, 0xa000, v194
	global_load_dwordx4 v[124:127], v107, s[14:15]
	v_add_u32_e32 v106, 0xc000, v194
	global_load_dwordx4 v[128:131], v106, s[14:15]
	v_add_u32_e32 v107, 0xe000, v194
	global_load_dwordx4 v[132:135], v107, s[14:15]
	v_add_u32_e32 v106, 0x10000, v194
	global_load_dwordx4 v[136:139], v106, s[14:15]
	v_add_u32_e32 v107, 0x12000, v194
	global_load_dwordx4 v[140:143], v107, s[14:15]
	v_add_u32_e32 v106, 0x14000, v194
	global_load_dwordx4 v[158:161], v106, s[14:15]
	v_add_u32_e32 v107, 0x16000, v194
	global_load_dwordx4 v[170:173], v107, s[14:15]
	v_add_u32_e32 v106, 0x18000, v194
	global_load_dwordx4 v[186:189], v106, s[14:15]
	v_add_u32_e32 v107, 0x1a000, v194
	global_load_dwordx4 v[190:193], v107, s[14:15]
	v_add_u32_e32 v106, 0x1c000, v194
	global_load_dwordx4 v[204:207], v106, s[14:15]
	v_add_u32_e32 v107, 0x1e000, v194
	global_load_dwordx4 v[208:211], v107, s[14:15]
	v_add_u32_e32 v106, 0x20000, v194
	global_load_dwordx4 v[212:215], v106, s[14:15]
	v_add_u32_e32 v107, 0x22000, v194
	global_load_dwordx4 v[216:219], v107, s[14:15]
	v_add_u32_e32 v106, 0x24000, v194
	global_load_dwordx4 v[220:223], v106, s[14:15]
	v_add_u32_e32 v107, 0x26000, v194
	global_load_dwordx4 v[112:115], v107, s[14:15]
	v_add_u32_e32 v224, 0x400, v196
	s_movk_i32 s0, 0x1c00
	v_and_or_b32 v224, v224, s0, v203
	buffer_load_dwordx4 v[62:65], v224, s[4:7], 0 offen nt
	v_or_b32_e32 v227, 0x2000, v224
	buffer_load_dwordx4 v[38:41], v227, s[4:7], 0 offen nt
	v_or_b32_e32 v226, 0x4000, v224
	buffer_load_dwordx4 v[42:45], v226, s[4:7], 0 offen nt
	v_or_b32_e32 v227, 0x6000, v224
	buffer_load_dwordx4 v[14:17], v227, s[4:7], 0 offen nt
	v_or_b32_e32 v226, 0x8000, v224
	buffer_load_dwordx4 v[46:49], v226, s[4:7], 0 offen nt
	v_or_b32_e32 v227, 0xa000, v224
	buffer_load_dwordx4 v[18:21], v227, s[4:7], 0 offen nt
	v_or_b32_e32 v226, 0xc000, v224
	buffer_load_dwordx4 v[50:53], v226, s[4:7], 0 offen nt
	v_or_b32_e32 v227, 0xe000, v224
	buffer_load_dwordx4 v[22:25], v227, s[4:7], 0 offen nt
	v_or_b32_e32 v226, 0x10000, v224
	buffer_load_dwordx4 v[54:57], v226, s[4:7], 0 offen nt
	v_or_b32_e32 v227, 0x12000, v224
	buffer_load_dwordx4 v[26:29], v227, s[4:7], 0 offen nt
	v_or_b32_e32 v226, 0x14000, v224
	buffer_load_dwordx4 v[58:61], v226, s[4:7], 0 offen nt
	v_or_b32_e32 v227, 0x16000, v224
	buffer_load_dwordx4 v[30:33], v227, s[4:7], 0 offen nt
	v_or_b32_e32 v226, 0x18000, v224
	buffer_load_dwordx4 v[34:37], v226, s[4:7], 0 offen nt
	v_or_b32_e32 v227, 0x1a000, v224
	buffer_load_dwordx4 v[6:9], v227, s[4:7], 0 offen nt
	v_or_b32_e32 v226, 0x1c000, v224
	buffer_load_dwordx4 v[10:13], v226, s[4:7], 0 offen nt
	v_or_b32_e32 v227, 0x1e000, v224
	buffer_load_dwordx4 v[2:5], v227, s[4:7], 0 offen nt
	s_mov_b32 s1, 0xe000
	s_mov_b32 s10, 0xa000
	s_mov_b32 s11, 0x6000
	s_mov_b32 s12, 0xc000
	s_mov_b32 s13, 0x8000
	s_mov_b32 s14, 0x1e000
	s_mov_b32 s15, 0x1c000
	s_mov_b32 s16, 0x2000
	s_mov_b32 s17, 0x4000
	s_mov_b32 s18, 0x10000
	s_mov_b32 s19, 0x1a000
	s_mov_b32 s20, 0x18000
	s_mov_b32 s21, 0x16000
	s_mov_b32 s22, 0x14000
	s_mov_b32 s23, 0x12000
	s_mov_b32 s24, 0xe0
	s_mov_b32 s26, 0x3e13bb63
	v_lshrrev_b32_e32 v144, 3, v0
	v_bfe_u32 v145, v0, 1, 2
	v_lshlrev_b32_e32 v108, 3, v0
	v_and_b32_e32 v109, 8, v108
	v_lshlrev_b32_e32 v224, 8, v144
	v_lshlrev_b32_e32 v225, 6, v145
	v_lshlrev_b32_e32 v226, 8, v145
	v_lshlrev_b32_e32 v110, 10, v144
	v_or3_b32 v110, v226, v110, v109
	v_or3_b32 v111, v224, v225, v109
	v_add_u32_e32 v111, 0xff00, v111
	v_add_u32_e32 v144, 0x24800, v194
	v_bfe_u32 v201, v0, 4, 2
	v_and_b32_e32 v197, 15, v0
	v_lshlrev_b32_e32 v202, 2, v201
	s_waitcnt vmcnt(34)
	v_pk_add_f32 v[224:225], v[228:229], 0 op_sel_hi:[1,0]
	v_pk_add_f32 v[226:227], v[230:231], 0 op_sel_hi:[1,0]
	v_cvt_pk_bf16_f32 v228, v228, v229
	v_cvt_pk_bf16_f32 v229, v230, v231
	v_pk_add_f32 v[224:225], v[224:225], v[98:99]
	v_pk_add_f32 v[226:227], v[226:227], v[100:101]
	v_cvt_pk_bf16_f32 v98, v98, v99
	v_cvt_pk_bf16_f32 v99, v100, v101
	ds_write2_b64 v110, v[228:229], v[98:99] offset1:2
	s_waitcnt vmcnt(32)
	v_pk_add_f32 v[224:225], v[224:225], v[102:103]
	v_pk_add_f32 v[226:227], v[226:227], v[104:105]
	v_cvt_pk_bf16_f32 v102, v102, v103
	v_cvt_pk_bf16_f32 v103, v104, v105
	v_pk_add_f32 v[224:225], v[224:225], v[116:117]
	v_pk_add_f32 v[226:227], v[226:227], v[118:119]
	v_cvt_pk_bf16_f32 v116, v116, v117
	v_cvt_pk_bf16_f32 v117, v118, v119
	ds_write2_b64 v110, v[102:103], v[116:117] offset0:4 offset1:6
	s_waitcnt vmcnt(30)
	v_pk_add_f32 v[224:225], v[224:225], v[120:121]
	v_pk_add_f32 v[226:227], v[226:227], v[122:123]
	v_cvt_pk_bf16_f32 v120, v120, v121
	v_cvt_pk_bf16_f32 v121, v122, v123
	v_pk_add_f32 v[224:225], v[224:225], v[124:125]
	v_pk_add_f32 v[226:227], v[226:227], v[126:127]
	v_cvt_pk_bf16_f32 v124, v124, v125
	v_cvt_pk_bf16_f32 v125, v126, v127
	ds_write2_b64 v110, v[120:121], v[124:125] offset0:8 offset1:10
	s_waitcnt vmcnt(28)
	v_pk_add_f32 v[224:225], v[224:225], v[128:129]
	v_pk_add_f32 v[226:227], v[226:227], v[130:131]
	v_cvt_pk_bf16_f32 v128, v128, v129
	v_cvt_pk_bf16_f32 v129, v130, v131
	v_pk_add_f32 v[224:225], v[224:225], v[132:133]
	v_pk_add_f32 v[226:227], v[226:227], v[134:135]
	v_cvt_pk_bf16_f32 v132, v132, v133
	v_cvt_pk_bf16_f32 v133, v134, v135
	ds_write2_b64 v110, v[128:129], v[132:133] offset0:12 offset1:14
	s_waitcnt vmcnt(26)
	v_pk_add_f32 v[224:225], v[224:225], v[136:137]
	v_pk_add_f32 v[226:227], v[226:227], v[138:139]
	v_cvt_pk_bf16_f32 v136, v136, v137
	v_cvt_pk_bf16_f32 v137, v138, v139
	v_pk_add_f32 v[224:225], v[224:225], v[140:141]
	v_pk_add_f32 v[226:227], v[226:227], v[142:143]
	v_cvt_pk_bf16_f32 v140, v140, v141
	v_cvt_pk_bf16_f32 v141, v142, v143
	ds_write2_b64 v110, v[136:137], v[140:141] offset0:16 offset1:18
	s_waitcnt vmcnt(24)
	v_pk_add_f32 v[224:225], v[224:225], v[158:159]
	v_pk_add_f32 v[226:227], v[226:227], v[160:161]
	v_cvt_pk_bf16_f32 v158, v158, v159
	v_cvt_pk_bf16_f32 v159, v160, v161
	v_pk_add_f32 v[224:225], v[224:225], v[170:171]
	v_pk_add_f32 v[226:227], v[226:227], v[172:173]
	v_cvt_pk_bf16_f32 v170, v170, v171
	v_cvt_pk_bf16_f32 v171, v172, v173
	ds_write2_b64 v110, v[158:159], v[170:171] offset0:20 offset1:22
	s_waitcnt vmcnt(22)
	v_pk_add_f32 v[224:225], v[224:225], v[186:187]
	v_pk_add_f32 v[226:227], v[226:227], v[188:189]
	v_cvt_pk_bf16_f32 v186, v186, v187
	v_cvt_pk_bf16_f32 v187, v188, v189
	v_pk_add_f32 v[224:225], v[224:225], v[190:191]
	v_pk_add_f32 v[226:227], v[226:227], v[192:193]
	v_cvt_pk_bf16_f32 v190, v190, v191
	v_cvt_pk_bf16_f32 v191, v192, v193
	ds_write2_b64 v110, v[186:187], v[190:191] offset0:24 offset1:26
	s_waitcnt vmcnt(20)
	v_pk_add_f32 v[224:225], v[224:225], v[204:205]
	v_pk_add_f32 v[226:227], v[226:227], v[206:207]
	v_cvt_pk_bf16_f32 v204, v204, v205
	v_cvt_pk_bf16_f32 v205, v206, v207
	v_pk_add_f32 v[224:225], v[224:225], v[208:209]
	v_pk_add_f32 v[226:227], v[226:227], v[210:211]
	v_cvt_pk_bf16_f32 v208, v208, v209
	v_cvt_pk_bf16_f32 v209, v210, v211
	ds_write2_b64 v110, v[204:205], v[208:209] offset0:28 offset1:30
	s_waitcnt vmcnt(18)
	v_pk_add_f32 v[224:225], v[224:225], v[212:213]
	v_pk_add_f32 v[226:227], v[226:227], v[214:215]
	v_cvt_pk_bf16_f32 v212, v212, v213
	v_cvt_pk_bf16_f32 v213, v214, v215
	v_pk_add_f32 v[224:225], v[224:225], v[216:217]
	v_pk_add_f32 v[226:227], v[226:227], v[218:219]
	v_cvt_pk_bf16_f32 v216, v216, v217
	v_cvt_pk_bf16_f32 v217, v218, v219
	ds_write2_b64 v111, v[212:213], v[216:217] offset0:32 offset1:34
	s_waitcnt vmcnt(16)
	v_pk_add_f32 v[224:225], v[224:225], v[220:221]
	v_pk_add_f32 v[226:227], v[226:227], v[222:223]
	v_cvt_pk_bf16_f32 v220, v220, v221
	v_cvt_pk_bf16_f32 v221, v222, v223
	v_pk_add_f32 v[224:225], v[224:225], v[112:113]
	v_pk_add_f32 v[226:227], v[226:227], v[114:115]
	v_cvt_pk_bf16_f32 v112, v112, v113
	v_cvt_pk_bf16_f32 v113, v114, v115
	ds_write2_b64 v111, v[220:221], v[112:113] offset0:36 offset1:38
	v_pk_mul_f32 v[224:225], v[224:225], s[26:27] op_sel_hi:[1,0]
	v_pk_mul_f32 v[226:227], v[226:227], s[26:27] op_sel_hi:[1,0]
	ds_write_b128 v144, v[224:227]
	v_and_or_b32 v98, v0, 3, v202
	v_mov_b32_e32 v99, 0x10000
	v_lshl_or_b32 v204, v98, 4, v99
	s_movk_i32 s25, 0x2100
	v_mov_b32_e32 v98, 0x14000
	v_mad_u32_u24 v199, v200, s25, v98
	v_add_u32_e32 v98, 0x800, v196
	v_and_or_b32 v186, v98, s0, v203
	v_or_b32_e32 v98, 0x2000, v186
	s_waitcnt lgkmcnt(0)
	s_barrier
	buffer_load_dwordx4 v[102:105], v186, s[4:7], 0 offen nt
	s_nop 0
	buffer_load_dwordx4 v[98:101], v98, s[4:7], 0 offen nt
	v_or_b32_e32 v106, 0x4000, v186
	v_or_b32_e32 v107, 0x6000, v186
	v_or_b32_e32 v114, 0x8000, v186
	v_or_b32_e32 v115, 0xa000, v186
	v_or_b32_e32 v122, 0xc000, v186
	v_or_b32_e32 v123, 0xe000, v186
	v_or_b32_e32 v130, 0x10000, v186
	v_or_b32_e32 v131, 0x12000, v186
	v_or_b32_e32 v138, 0x14000, v186
	v_or_b32_e32 v139, 0x16000, v186
	v_or_b32_e32 v158, 0x18000, v186
	v_or_b32_e32 v159, 0x1a000, v186
	v_or_b32_e32 v187, 0x1c000, v186
	v_or_b32_e32 v186, 0x1e000, v186
	v_or_b32_e32 v213, v199, v109
	v_and_b32_e32 v214, 0x1f0, v108
	buffer_load_dwordx4 v[110:113], v106, s[4:7], 0 offen nt
	s_nop 0
	buffer_load_dwordx4 v[106:109], v107, s[4:7], 0 offen nt
	s_nop 0
	buffer_load_dwordx4 v[118:121], v114, s[4:7], 0 offen nt
	s_nop 0
	buffer_load_dwordx4 v[114:117], v115, s[4:7], 0 offen nt
	s_nop 0
	buffer_load_dwordx4 v[126:129], v122, s[4:7], 0 offen nt
	s_nop 0
	buffer_load_dwordx4 v[122:125], v123, s[4:7], 0 offen nt
	s_nop 0
	buffer_load_dwordx4 v[134:137], v130, s[4:7], 0 offen nt
	s_nop 0
	buffer_load_dwordx4 v[130:133], v131, s[4:7], 0 offen nt
	s_nop 0
	buffer_load_dwordx4 v[142:145], v138, s[4:7], 0 offen nt
	s_nop 0
	buffer_load_dwordx4 v[138:141], v139, s[4:7], 0 offen nt
	s_nop 0
	buffer_load_dwordx4 v[170:173], v158, s[4:7], 0 offen nt
	s_nop 0
	buffer_load_dwordx4 v[158:161], v159, s[4:7], 0 offen nt
	s_nop 0
	buffer_load_dwordx4 v[190:193], v187, s[4:7], 0 offen nt
	s_nop 0
	buffer_load_dwordx4 v[186:189], v186, s[4:7], 0 offen nt
	s_waitcnt vmcnt(32)
	v_cvt_pk_bf16_f32 v66, v66, v67
	v_cvt_pk_bf16_f32 v67, v68, v69
	s_movk_i32 s25, 0x50
	v_xad_u32 v207, v214, s25, v213
	s_movk_i32 s25, 0x60
	v_xad_u32 v206, v214, s25, v213
	s_movk_i32 s25, 0x70
	v_xad_u32 v205, v214, s25, v213
	s_movk_i32 s25, 0x80
	v_xad_u32 v211, v214, 16, v213
	v_xad_u32 v231, v214, s25, v213
	s_movk_i32 s25, 0x90
	v_xad_u32 v210, v214, 32, v213
	v_xad_u32 v230, v214, s25, v213
	s_movk_i32 s25, 0xa0
	ds_write_b64 v211, v[66:67] offset:512
	v_cvt_pk_bf16_f32 v66, v78, v79
	v_cvt_pk_bf16_f32 v67, v80, v81
	v_xad_u32 v209, v214, 48, v213
	v_xad_u32 v229, v214, s25, v213
	s_movk_i32 s25, 0xb0
	ds_write_b64 v210, v[66:67] offset:1024
	v_cvt_pk_bf16_f32 v66, v74, v75
	v_cvt_pk_bf16_f32 v67, v76, v77
	v_xad_u32 v208, v214, 64, v213
	v_xad_u32 v228, v214, s25, v213
	s_movk_i32 s25, 0xc0
	ds_write_b64 v209, v[66:67] offset:1536
	v_cvt_pk_bf16_f32 v66, v86, v87
	v_cvt_pk_bf16_f32 v67, v88, v89
	v_xad_u32 v227, v214, s25, v213
	s_movk_i32 s25, 0xd0
	v_xad_u32 v225, v214, s24, v213
	s_movk_i32 s24, 0xf0
	ds_write_b64 v208, v[66:67] offset:2048
	v_cvt_pk_bf16_f32 v66, v82, v83
	v_cvt_pk_bf16_f32 v67, v84, v85
	v_add_u32_e32 v212, v213, v214
	v_xad_u32 v226, v214, s25, v213
	v_xad_u32 v224, v214, s24, v213
	v_lshl_add_u32 v213, v197, 9, v199
	v_bitop3_b32 v214, v201, v0, 15 bitop3:0x78
	ds_write_b64 v207, v[66:67] offset:2560
	v_cvt_pk_bf16_f32 v66, v94, v95
	v_cvt_pk_bf16_f32 v67, v96, v97
	v_lshl_or_b32 v223, v214, 4, v213
	v_bitop3_b32 v214, v201, v197, 4 bitop3:0x36
	ds_write_b64 v206, v[66:67] offset:3072
	v_cvt_pk_bf16_f32 v66, v90, v91
	v_cvt_pk_bf16_f32 v67, v92, v93
	v_lshl_or_b32 v222, v214, 4, v213
	v_bitop3_b32 v214, v201, v197, 8 bitop3:0x36
	ds_write_b64 v205, v[66:67] offset:3584
	v_cvt_pk_bf16_f32 v66, v150, v151
	v_cvt_pk_bf16_f32 v67, v152, v153
	v_lshl_or_b32 v221, v214, 4, v213
	v_bitop3_b32 v214, v201, v197, 12 bitop3:0x36
	ds_write_b64 v231, v[66:67] offset:4096
	v_cvt_pk_bf16_f32 v66, v146, v147
	v_cvt_pk_bf16_f32 v67, v148, v149
	v_lshl_or_b32 v219, v214, 4, v213
	v_bitop3_b32 v214, v201, v197, 16 bitop3:0x36
	ds_write_b64 v230, v[66:67] offset:4608
	v_cvt_pk_bf16_f32 v66, v162, v163
	v_cvt_pk_bf16_f32 v67, v164, v165
	v_lshl_add_u32 v218, v214, 4, v213
	v_bitop3_b32 v214, v201, v197, 20 bitop3:0x36
	ds_write_b64 v229, v[66:67] offset:5120
	v_cvt_pk_bf16_f32 v66, v154, v155
	v_cvt_pk_bf16_f32 v67, v156, v157
	v_lshl_add_u32 v217, v214, 4, v213
	v_bitop3_b32 v214, v201, v197, 24 bitop3:0x36
	ds_write_b64 v228, v[66:67] offset:5632
	v_cvt_pk_bf16_f32 v66, v174, v175
	v_cvt_pk_bf16_f32 v67, v176, v177
	v_lshl_add_u32 v216, v214, 4, v213
	v_bitop3_b32 v214, v201, v197, 28 bitop3:0x36
	ds_write_b64 v227, v[66:67] offset:6144
	v_cvt_pk_bf16_f32 v66, v166, v167
	v_cvt_pk_bf16_f32 v67, v168, v169
	v_add_u32_e32 v235, 3, v200
	v_lshl_add_u32 v213, v214, 4, v213
	ds_write_b64 v226, v[66:67] offset:6656
	v_cvt_pk_bf16_f32 v66, v182, v183
	v_cvt_pk_bf16_f32 v67, v184, v185
	v_cvt_pk_bf16_f32 v70, v70, v71
	v_cvt_pk_bf16_f32 v71, v72, v73
	ds_write_b64 v212, v[70:71]
	ds_write_b64 v225, v[66:67] offset:7168
	v_cvt_pk_bf16_f32 v66, v178, v179
	v_cvt_pk_bf16_f32 v67, v180, v181
	ds_write_b64 v224, v[66:67] offset:7680
	v_lshl_or_b32 v66, v200, 13, v198
	ds_read_b128 v[66:69], v66
	v_lshlrev_b32_e32 v220, 11, v200
	v_or_b32_e32 v70, v204, v220
	ds_read_b128 v[70:73], v70
	ds_read_b128 v[74:77], v223
	v_lshlrev_b32_e32 v232, 3, v200
	v_or_b32_e32 v214, 1, v232
	s_waitcnt lgkmcnt(0)
	v_mfma_f32_16x16x32_bf16 v[70:73], v[70:73], v[74:77], 0
	v_lshlrev_b32_e32 v215, 8, v214
	v_or_b32_e32 v78, v204, v215
	v_or_b32_e32 v184, 2, v232
	v_mfma_f32_16x16x32_bf16 v[66:69], v[66:69], v[74:77], 0
	v_lshl_or_b32 v74, v214, 10, v198
	ds_read_b128 v[74:77], v74
	ds_read_b128 v[78:81], v78
	ds_read_b128 v[82:85], v222
	v_lshlrev_b32_e32 v185, 8, v184
	s_waitcnt lgkmcnt(0)
	v_mfma_f32_16x16x32_bf16 v[70:73], v[78:81], v[82:85], v[70:73]
	v_or_b32_e32 v78, v204, v185
	v_or_b32_e32 v182, 3, v232
	v_lshlrev_b32_e32 v183, 8, v182
	v_mfma_f32_16x16x32_bf16 v[66:69], v[74:77], v[82:85], v[66:69]
	v_lshl_or_b32 v74, v184, 10, v198
	ds_read_b128 v[74:77], v74
	ds_read_b128 v[78:81], v78
	ds_read_b128 v[82:85], v221
	s_waitcnt lgkmcnt(0)
	v_mfma_f32_16x16x32_bf16 v[70:73], v[78:81], v[82:85], v[70:73]
	v_or_b32_e32 v78, v204, v183
	v_or_b32_e32 v180, 4, v232
	v_lshlrev_b32_e32 v181, 8, v180
	v_mfma_f32_16x16x32_bf16 v[66:69], v[74:77], v[82:85], v[66:69]
	v_lshl_or_b32 v74, v182, 10, v198
	ds_read_b128 v[74:77], v74
	ds_read_b128 v[78:81], v78
	ds_read_b128 v[82:85], v219
	s_waitcnt lgkmcnt(0)
	v_mfma_f32_16x16x32_bf16 v[66:69], v[74:77], v[82:85], v[66:69]
	v_lshl_or_b32 v74, v180, 10, v198
	ds_read_b128 v[74:77], v74
	v_or_b32_e32 v178, 5, v232
	v_mfma_f32_16x16x32_bf16 v[70:73], v[78:81], v[82:85], v[70:73]
	v_or_b32_e32 v78, v204, v181
	ds_read_b128 v[78:81], v78
	ds_read_b128 v[82:85], v218
	v_lshlrev_b32_e32 v179, 8, v178
	s_waitcnt lgkmcnt(0)
	v_mfma_f32_16x16x32_bf16 v[66:69], v[74:77], v[82:85], v[66:69]
	v_lshl_or_b32 v74, v178, 10, v198
	ds_read_b128 v[74:77], v74
	v_or_b32_e32 v176, 6, v232
	v_mfma_f32_16x16x32_bf16 v[70:73], v[78:81], v[82:85], v[70:73]
	v_or_b32_e32 v78, v204, v179
	ds_read_b128 v[78:81], v78
	ds_read_b128 v[82:85], v217
	v_lshlrev_b32_e32 v177, 8, v176
	s_waitcnt lgkmcnt(0)
	v_mfma_f32_16x16x32_bf16 v[66:69], v[74:77], v[82:85], v[66:69]
	v_lshl_or_b32 v74, v176, 10, v198
	ds_read_b128 v[74:77], v74
	v_or_b32_e32 v174, 7, v232
	v_mfma_f32_16x16x32_bf16 v[70:73], v[78:81], v[82:85], v[70:73]
	v_or_b32_e32 v78, v204, v177
	ds_read_b128 v[78:81], v78
	ds_read_b128 v[82:85], v216
	v_lshlrev_b32_e32 v175, 8, v174
	s_waitcnt lgkmcnt(0)
	v_mfma_f32_16x16x32_bf16 v[66:69], v[74:77], v[82:85], v[66:69]
	v_lshl_or_b32 v74, v174, 10, v198
	s_waitcnt vmcnt(16)
	v_cvt_pk_bf16_f32 v14, v14, v15
	v_cvt_pk_bf16_f32 v15, v16, v17
	v_mfma_f32_16x16x32_bf16 v[70:73], v[78:81], v[82:85], v[70:73]
	v_or_b32_e32 v78, v204, v175
	ds_read_b128 v[74:77], v74
	ds_read_b128 v[78:81], v78
	ds_read_b128 v[82:85], v213
	ds_write_b64 v209, v[14:15] offset:1536
	v_cvt_pk_bf16_f32 v14, v46, v47
	v_cvt_pk_bf16_f32 v15, v48, v49
	ds_write_b64 v208, v[14:15] offset:2048
	v_cvt_pk_bf16_f32 v14, v18, v19
	v_cvt_pk_bf16_f32 v15, v20, v21
	ds_write_b64 v207, v[14:15] offset:2560
	v_cvt_pk_bf16_f32 v14, v50, v51
	v_cvt_pk_bf16_f32 v15, v52, v53
	ds_write_b64 v206, v[14:15] offset:3072
	v_cvt_pk_bf16_f32 v14, v22, v23
	v_cvt_pk_bf16_f32 v15, v24, v25
	ds_write_b64 v205, v[14:15] offset:3584
	v_cvt_pk_bf16_f32 v14, v54, v55
	v_cvt_pk_bf16_f32 v15, v56, v57
	v_cvt_pk_bf16_f32 v6, v6, v7
	v_cvt_pk_bf16_f32 v2, v2, v3
	ds_write_b64 v231, v[14:15] offset:4096
	v_cvt_pk_bf16_f32 v14, v26, v27
	v_cvt_pk_bf16_f32 v15, v28, v29
	v_cvt_pk_bf16_f32 v7, v8, v9
	ds_write_b64 v226, v[6:7] offset:6656
	v_cvt_pk_bf16_f32 v6, v10, v11
	v_cvt_pk_bf16_f32 v3, v4, v5
	ds_write_b64 v224, v[2:3] offset:7680
	v_lshlrev_b32_e32 v2, 10, v235
	ds_write_b64 v230, v[14:15] offset:4608
	v_cvt_pk_bf16_f32 v14, v58, v59
	v_cvt_pk_bf16_f32 v15, v60, v61
	v_cvt_pk_bf16_f32 v7, v12, v13
	ds_write_b64 v225, v[6:7] offset:7168
	v_and_or_b32 v6, v2, s0, v203
	ds_write_b64 v229, v[14:15] offset:5120
	v_cvt_pk_bf16_f32 v14, v30, v31
	v_cvt_pk_bf16_f32 v15, v32, v33
	v_or_b32_e32 v7, 0x2000, v6
	ds_write_b64 v228, v[14:15] offset:5632
	v_cvt_pk_bf16_f32 v14, v34, v35
	v_cvt_pk_bf16_f32 v15, v36, v37
	buffer_load_dwordx4 v[2:5], v6, s[4:7], 0 offen nt
	buffer_load_dwordx4 v[10:13], v7, s[4:7], 0 offen nt
	v_or_b32_e32 v7, 0x4000, v6
	ds_write_b64 v227, v[14:15] offset:6144
	buffer_load_dwordx4 v[14:17], v7, s[4:7], 0 offen nt
	v_or_b32_e32 v7, 0x6000, v6
	v_cvt_pk_bf16_f32 v38, v38, v39
	v_cvt_pk_bf16_f32 v39, v40, v41
	buffer_load_dwordx4 v[22:25], v7, s[4:7], 0 offen nt
	v_or_b32_e32 v7, 0x8000, v6
	ds_write_b64 v211, v[38:39] offset:512
	v_cvt_pk_bf16_f32 v38, v42, v43
	v_cvt_pk_bf16_f32 v39, v44, v45
	buffer_load_dwordx4 v[30:33], v7, s[4:7], 0 offen nt
	v_or_b32_e32 v7, 0xa000, v6
	ds_write_b64 v210, v[38:39] offset:1024
	buffer_load_dwordx4 v[38:41], v7, s[4:7], 0 offen nt
	v_or_b32_e32 v7, 0xc000, v6
	buffer_load_dwordx4 v[46:49], v7, s[4:7], 0 offen nt
	v_or_b32_e32 v7, 0xe000, v6
	v_cvt_pk_bf16_f32 v62, v62, v63
	v_cvt_pk_bf16_f32 v63, v64, v65
	buffer_load_dwordx4 v[54:57], v7, s[4:7], 0 offen nt
	v_or_b32_e32 v7, 0x10000, v6
	ds_write_b64 v212, v[62:63]
	buffer_load_dwordx4 v[62:65], v7, s[4:7], 0 offen nt
	v_or_b32_e32 v7, 0x12000, v6
	s_waitcnt lgkmcnt(14)
	v_mfma_f32_16x16x32_bf16 v[66:69], v[74:77], v[82:85], v[66:69]
	v_mfma_f32_16x16x32_bf16 v[74:77], v[78:81], v[82:85], v[70:73]
	s_nop 2
	buffer_load_dwordx4 v[70:73], v7, s[4:7], 0 offen nt
	v_or_b32_e32 v7, 0x14000, v6
	buffer_load_dwordx4 v[78:81], v7, s[4:7], 0 offen nt
	v_or_b32_e32 v7, 0x16000, v6
	buffer_load_dwordx4 v[86:89], v7, s[4:7], 0 offen nt
	v_or_b32_e32 v7, 0x18000, v6
	buffer_load_dwordx4 v[94:97], v7, s[4:7], 0 offen nt
	v_or_b32_e32 v7, 0x1a000, v6
	buffer_load_dwordx4 v[146:149], v7, s[4:7], 0 offen nt
	v_or_b32_e32 v7, 0x1c000, v6
	v_or_b32_e32 v6, 0x1e000, v6
	buffer_load_dwordx4 v[150:153], v7, s[4:7], 0 offen nt
	buffer_load_dwordx4 v[154:157], v6, s[4:7], 0 offen nt
	v_add_u32_e32 v6, 8, v232
	v_and_b32_e32 v50, 56, v6
	v_lshl_or_b32 v6, v50, 10, v198
	ds_read_b128 v[6:9], v6
	v_lshl_or_b32 v18, v50, 8, v204
	ds_read_b128 v[18:21], v18
	ds_read_b128 v[26:29], v223
	v_or_b32_e32 v34, 1, v50
	s_movk_i32 s24, 0x1000
	s_waitcnt lgkmcnt(0)
	v_mfma_f32_16x16x32_bf16 v[18:21], v[18:21], v[26:29], v[74:77]
	v_add_u32_e32 v234, 5, v200
	v_mfma_f32_16x16x32_bf16 v[6:9], v[6:9], v[26:29], v[66:69]
	v_lshl_or_b32 v26, v34, 10, v198
	ds_read_b128 v[26:29], v26
	v_lshl_or_b32 v34, v34, 8, v204
	ds_read_b128 v[34:37], v34
	ds_read_b128 v[42:45], v222
	s_waitcnt lgkmcnt(0)
	v_mfma_f32_16x16x32_bf16 v[18:21], v[34:37], v[42:45], v[18:21]
	v_or_b32_e32 v34, 2, v50
	v_mfma_f32_16x16x32_bf16 v[6:9], v[26:29], v[42:45], v[6:9]
	v_lshl_or_b32 v26, v34, 10, v198
	ds_read_b128 v[26:29], v26
	v_lshl_or_b32 v34, v34, 8, v204
	ds_read_b128 v[34:37], v34
	ds_read_b128 v[42:45], v221
	s_waitcnt lgkmcnt(0)
	v_mfma_f32_16x16x32_bf16 v[18:21], v[34:37], v[42:45], v[18:21]
	v_or_b32_e32 v34, 3, v50
	v_mfma_f32_16x16x32_bf16 v[6:9], v[26:29], v[42:45], v[6:9]
	v_lshl_or_b32 v26, v34, 10, v198
	ds_read_b128 v[26:29], v26
	v_lshl_or_b32 v34, v34, 8, v204
	ds_read_b128 v[34:37], v34
	ds_read_b128 v[42:45], v219
	s_waitcnt lgkmcnt(0)
	v_mfma_f32_16x16x32_bf16 v[18:21], v[34:37], v[42:45], v[18:21]
	v_or_b32_e32 v34, 4, v50
	v_mfma_f32_16x16x32_bf16 v[6:9], v[26:29], v[42:45], v[6:9]
	v_lshl_or_b32 v26, v34, 10, v198
	ds_read_b128 v[26:29], v26
	v_lshl_or_b32 v34, v34, 8, v204
	ds_read_b128 v[34:37], v34
	ds_read_b128 v[42:45], v218
	s_waitcnt lgkmcnt(0)
	v_mfma_f32_16x16x32_bf16 v[18:21], v[34:37], v[42:45], v[18:21]
	v_or_b32_e32 v34, 5, v50
	v_mfma_f32_16x16x32_bf16 v[6:9], v[26:29], v[42:45], v[6:9]
	v_lshl_or_b32 v26, v34, 10, v198
	ds_read_b128 v[26:29], v26
	v_lshl_or_b32 v34, v34, 8, v204
	ds_read_b128 v[34:37], v34
	ds_read_b128 v[42:45], v217
	s_waitcnt lgkmcnt(0)
	v_mfma_f32_16x16x32_bf16 v[18:21], v[34:37], v[42:45], v[18:21]
	v_or_b32_e32 v34, 6, v50
	v_mfma_f32_16x16x32_bf16 v[6:9], v[26:29], v[42:45], v[6:9]
	v_lshl_or_b32 v26, v34, 10, v198
	ds_read_b128 v[26:29], v26
	v_lshl_or_b32 v34, v34, 8, v204
	ds_read_b128 v[34:37], v34
	ds_read_b128 v[42:45], v216
	s_waitcnt lgkmcnt(0)
	v_mfma_f32_16x16x32_bf16 v[18:21], v[34:37], v[42:45], v[18:21]
	v_or_b32_e32 v34, 7, v50
	v_mfma_f32_16x16x32_bf16 v[6:9], v[26:29], v[42:45], v[6:9]
	v_lshl_or_b32 v26, v34, 10, v198
	ds_read_b128 v[26:29], v26
	v_lshl_or_b32 v34, v34, 8, v204
	ds_read_b128 v[34:37], v34
	ds_read_b128 v[42:45], v213
	s_waitcnt lgkmcnt(0)
	v_mfma_f32_16x16x32_bf16 v[162:165], v[26:29], v[42:45], v[6:9]
	s_waitcnt vmcnt(31)
	s_nop 1
	v_cvt_pk_bf16_f32 v6, v102, v103
	v_cvt_pk_bf16_f32 v7, v104, v105
	ds_write_b64 v212, v[6:7]
	s_waitcnt vmcnt(30)
	v_cvt_pk_bf16_f32 v6, v98, v99
	v_cvt_pk_bf16_f32 v7, v100, v101
	ds_write_b64 v211, v[6:7] offset:512
	s_waitcnt vmcnt(29)
	v_cvt_pk_bf16_f32 v6, v110, v111
	v_cvt_pk_bf16_f32 v7, v112, v113
	ds_write_b64 v210, v[6:7] offset:1024
	s_waitcnt vmcnt(28)
	v_cvt_pk_bf16_f32 v6, v106, v107
	v_cvt_pk_bf16_f32 v7, v108, v109
	ds_write_b64 v209, v[6:7] offset:1536
	s_waitcnt vmcnt(27)
	v_cvt_pk_bf16_f32 v6, v118, v119
	v_cvt_pk_bf16_f32 v7, v120, v121
	ds_write_b64 v208, v[6:7] offset:2048
	s_waitcnt vmcnt(26)
	v_cvt_pk_bf16_f32 v6, v114, v115
	v_cvt_pk_bf16_f32 v7, v116, v117
	ds_write_b64 v207, v[6:7] offset:2560
	s_waitcnt vmcnt(25)
	v_cvt_pk_bf16_f32 v6, v126, v127
	v_cvt_pk_bf16_f32 v7, v128, v129
	ds_write_b64 v206, v[6:7] offset:3072
	s_waitcnt vmcnt(24)
	v_cvt_pk_bf16_f32 v6, v122, v123
	v_cvt_pk_bf16_f32 v7, v124, v125
	ds_write_b64 v205, v[6:7] offset:3584
	s_waitcnt vmcnt(23)
	v_cvt_pk_bf16_f32 v6, v134, v135
	v_cvt_pk_bf16_f32 v7, v136, v137
	ds_write_b64 v231, v[6:7] offset:4096
	s_waitcnt vmcnt(22)
	v_cvt_pk_bf16_f32 v6, v130, v131
	v_cvt_pk_bf16_f32 v7, v132, v133
	ds_write_b64 v230, v[6:7] offset:4608
	s_waitcnt vmcnt(21)
	v_cvt_pk_bf16_f32 v6, v142, v143
	v_cvt_pk_bf16_f32 v7, v144, v145
	ds_write_b64 v229, v[6:7] offset:5120
	s_waitcnt vmcnt(20)
	v_cvt_pk_bf16_f32 v6, v138, v139
	v_cvt_pk_bf16_f32 v7, v140, v141
	ds_write_b64 v228, v[6:7] offset:5632
	s_waitcnt vmcnt(19)
	v_cvt_pk_bf16_f32 v6, v170, v171
	v_cvt_pk_bf16_f32 v7, v172, v173
	ds_write_b64 v227, v[6:7] offset:6144
	s_waitcnt vmcnt(18)
	v_cvt_pk_bf16_f32 v6, v158, v159
	v_mov_b32_e32 v106, 0x1000
	v_cvt_pk_bf16_f32 v7, v160, v161
	ds_write_b64 v226, v[6:7] offset:6656
	s_waitcnt vmcnt(17)
	v_cvt_pk_bf16_f32 v6, v190, v191
	v_bitop3_b32 v107, v233, s19, v106 bitop3:0xde
	v_mfma_f32_16x16x32_bf16 v[166:169], v[34:37], v[42:45], v[18:21]
	v_cvt_pk_bf16_f32 v7, v192, v193
	ds_write_b64 v225, v[6:7] offset:7168
	s_waitcnt vmcnt(16)
	v_cvt_pk_bf16_f32 v6, v186, v187
	v_bitop3_b32 v26, v233, s17, v106 bitop3:0xde
	v_bitop3_b32 v34, v233, s11, v106 bitop3:0xde
	v_bitop3_b32 v18, v233, s16, v106 bitop3:0xde
	v_bitop3_b32 v42, v233, s13, v106 bitop3:0xde
	v_bitop3_b32 v50, v233, s10, v106 bitop3:0xde
	v_bitop3_b32 v58, v233, s12, v106 bitop3:0xde
	v_bitop3_b32 v66, v233, s1, v106 bitop3:0xde
	v_bitop3_b32 v74, v233, s18, v106 bitop3:0xde
	v_bitop3_b32 v82, v233, s23, v106 bitop3:0xde
	v_bitop3_b32 v90, v233, s22, v106 bitop3:0xde
	v_bitop3_b32 v98, v233, s21, v106 bitop3:0xde
	v_bitop3_b32 v102, v233, s20, v106 bitop3:0xde
	buffer_load_dwordx4 v[110:113], v107, s[4:7], 0 offen nt
	v_bitop3_b32 v107, v233, s15, v106 bitop3:0xde
	v_bitop3_b32 v106, v233, s14, v106 bitop3:0xde
	v_cvt_pk_bf16_f32 v7, v188, v189
	ds_write_b64 v224, v[6:7] offset:7680
	v_bitop3_b32 v6, v203, s24, v196 bitop3:0x36
	buffer_load_dwordx4 v[42:45], v42, s[4:7], 0 offen nt
	s_nop 0
	buffer_load_dwordx4 v[50:53], v50, s[4:7], 0 offen nt
	s_nop 0
	buffer_load_dwordx4 v[58:61], v58, s[4:7], 0 offen nt
	s_nop 0
	buffer_load_dwordx4 v[66:69], v66, s[4:7], 0 offen nt
	s_nop 0
	buffer_load_dwordx4 v[74:77], v74, s[4:7], 0 offen nt
	s_nop 0
	buffer_load_dwordx4 v[82:85], v82, s[4:7], 0 offen nt
	s_nop 0
	buffer_load_dwordx4 v[90:93], v90, s[4:7], 0 offen nt
	s_nop 0
	buffer_load_dwordx4 v[98:101], v98, s[4:7], 0 offen nt
	s_nop 0
	buffer_load_dwordx4 v[102:105], v102, s[4:7], 0 offen nt
	s_nop 0
	buffer_load_dwordx4 v[126:129], v106, s[4:7], 0 offen nt
	buffer_load_dwordx4 v[118:121], v107, s[4:7], 0 offen nt
	s_nop 0
	buffer_load_dwordx4 v[6:9], v6, s[4:7], 0 offen nt
	s_nop 0
	buffer_load_dwordx4 v[18:21], v18, s[4:7], 0 offen nt
	s_nop 0
	buffer_load_dwordx4 v[26:29], v26, s[4:7], 0 offen nt
	s_nop 0
	buffer_load_dwordx4 v[34:37], v34, s[4:7], 0 offen nt
	v_add_u32_e32 v106, 16, v232
	v_and_b32_e32 v138, 56, v106
	v_lshl_or_b32 v106, v138, 10, v198
	ds_read_b128 v[106:109], v106
	v_lshl_or_b32 v114, v138, 8, v204
	ds_read_b128 v[114:117], v114
	ds_read_b128 v[122:125], v223
	v_or_b32_e32 v130, 1, v138
	s_waitcnt vmcnt(31)
	v_cvt_pk_bf16_f32 v2, v2, v3
	s_waitcnt lgkmcnt(0)
	v_mfma_f32_16x16x32_bf16 v[114:117], v[114:117], v[122:125], v[166:169]
	v_cvt_pk_bf16_f32 v3, v4, v5
	v_mfma_f32_16x16x32_bf16 v[106:109], v[106:109], v[122:125], v[162:165]
	v_lshl_or_b32 v122, v130, 10, v198
	ds_read_b128 v[122:125], v122
	v_lshl_or_b32 v130, v130, 8, v204
	ds_read_b128 v[130:133], v130
	ds_read_b128 v[134:137], v222
	s_waitcnt lgkmcnt(0)
	v_mfma_f32_16x16x32_bf16 v[114:117], v[130:133], v[134:137], v[114:117]
	v_or_b32_e32 v130, 2, v138
	v_mfma_f32_16x16x32_bf16 v[106:109], v[122:125], v[134:137], v[106:109]
	v_lshl_or_b32 v122, v130, 10, v198
	ds_read_b128 v[122:125], v122
	v_lshl_or_b32 v130, v130, 8, v204
	ds_read_b128 v[130:133], v130
	ds_read_b128 v[134:137], v221
	s_waitcnt lgkmcnt(0)
	v_mfma_f32_16x16x32_bf16 v[114:117], v[130:133], v[134:137], v[114:117]
	v_or_b32_e32 v130, 3, v138
	v_mfma_f32_16x16x32_bf16 v[106:109], v[122:125], v[134:137], v[106:109]
	v_lshl_or_b32 v122, v130, 10, v198
	ds_read_b128 v[122:125], v122
	v_lshl_or_b32 v130, v130, 8, v204
	ds_read_b128 v[130:133], v130
	ds_read_b128 v[134:137], v219
	s_waitcnt lgkmcnt(0)
	v_mfma_f32_16x16x32_bf16 v[114:117], v[130:133], v[134:137], v[114:117]
	v_or_b32_e32 v130, 4, v138
	v_mfma_f32_16x16x32_bf16 v[106:109], v[122:125], v[134:137], v[106:109]
	v_lshl_or_b32 v122, v130, 10, v198
	ds_read_b128 v[122:125], v122
	v_lshl_or_b32 v130, v130, 8, v204
	ds_read_b128 v[130:133], v130
	ds_read_b128 v[134:137], v218
	s_waitcnt lgkmcnt(0)
	v_mfma_f32_16x16x32_bf16 v[114:117], v[130:133], v[134:137], v[114:117]
	v_or_b32_e32 v130, 5, v138
	v_mfma_f32_16x16x32_bf16 v[106:109], v[122:125], v[134:137], v[106:109]
	v_lshl_or_b32 v122, v130, 10, v198
	ds_read_b128 v[122:125], v122
	v_lshl_or_b32 v130, v130, 8, v204
	ds_read_b128 v[130:133], v130
	ds_read_b128 v[134:137], v217
	s_waitcnt lgkmcnt(0)
	v_mfma_f32_16x16x32_bf16 v[114:117], v[130:133], v[134:137], v[114:117]
	v_or_b32_e32 v130, 6, v138
	v_mfma_f32_16x16x32_bf16 v[106:109], v[122:125], v[134:137], v[106:109]
	v_lshl_or_b32 v122, v130, 10, v198
	ds_read_b128 v[122:125], v122
	v_lshl_or_b32 v130, v130, 8, v204
	ds_read_b128 v[130:133], v130
	ds_read_b128 v[134:137], v216
	s_waitcnt lgkmcnt(0)
	v_mfma_f32_16x16x32_bf16 v[114:117], v[130:133], v[134:137], v[114:117]
	v_or_b32_e32 v130, 7, v138
	v_mfma_f32_16x16x32_bf16 v[106:109], v[122:125], v[134:137], v[106:109]
	v_lshl_or_b32 v122, v130, 10, v198
	v_lshl_or_b32 v130, v130, 8, v204
	ds_read_b128 v[122:125], v122
	ds_read_b128 v[134:137], v130
	ds_read_b128 v[138:141], v213
	ds_write_b64 v212, v[2:3]
	s_waitcnt vmcnt(30)
	v_cvt_pk_bf16_f32 v2, v10, v11
	v_cvt_pk_bf16_f32 v3, v12, v13
	ds_write_b64 v211, v[2:3] offset:512
	s_waitcnt vmcnt(29)
	v_cvt_pk_bf16_f32 v2, v14, v15
	v_cvt_pk_bf16_f32 v3, v16, v17
	ds_write_b64 v210, v[2:3] offset:1024
	s_waitcnt vmcnt(28)
	v_cvt_pk_bf16_f32 v2, v22, v23
	v_cvt_pk_bf16_f32 v3, v24, v25
	ds_write_b64 v209, v[2:3] offset:1536
	s_waitcnt vmcnt(27)
	v_cvt_pk_bf16_f32 v2, v30, v31
	v_cvt_pk_bf16_f32 v3, v32, v33
	ds_write_b64 v208, v[2:3] offset:2048
	s_waitcnt vmcnt(26)
	v_cvt_pk_bf16_f32 v2, v38, v39
	v_cvt_pk_bf16_f32 v3, v40, v41
	ds_write_b64 v207, v[2:3] offset:2560
	s_waitcnt vmcnt(25)
	v_cvt_pk_bf16_f32 v2, v46, v47
	v_cvt_pk_bf16_f32 v3, v48, v49
	ds_write_b64 v206, v[2:3] offset:3072
	s_waitcnt vmcnt(24)
	v_cvt_pk_bf16_f32 v2, v54, v55
	v_cvt_pk_bf16_f32 v3, v56, v57
	ds_write_b64 v205, v[2:3] offset:3584
	s_waitcnt vmcnt(23)
	v_cvt_pk_bf16_f32 v2, v62, v63
	v_cvt_pk_bf16_f32 v3, v64, v65
	ds_write_b64 v231, v[2:3] offset:4096
	s_waitcnt vmcnt(22)
	v_cvt_pk_bf16_f32 v2, v70, v71
	v_cvt_pk_bf16_f32 v3, v72, v73
	ds_write_b64 v230, v[2:3] offset:4608
	s_waitcnt vmcnt(21)
	v_cvt_pk_bf16_f32 v2, v78, v79
	v_cvt_pk_bf16_f32 v3, v80, v81
	ds_write_b64 v229, v[2:3] offset:5120
	s_waitcnt vmcnt(20)
	v_cvt_pk_bf16_f32 v2, v86, v87
	v_cvt_pk_bf16_f32 v3, v88, v89
	ds_write_b64 v228, v[2:3] offset:5632
	s_waitcnt vmcnt(19)
	v_cvt_pk_bf16_f32 v2, v94, v95
	v_cvt_pk_bf16_f32 v3, v96, v97
	ds_write_b64 v227, v[2:3] offset:6144
	s_waitcnt vmcnt(18)
	v_cvt_pk_bf16_f32 v2, v146, v147
	v_cvt_pk_bf16_f32 v3, v148, v149
	ds_write_b64 v226, v[2:3] offset:6656
	s_waitcnt vmcnt(17)
	v_cvt_pk_bf16_f32 v2, v150, v151
	v_cvt_pk_bf16_f32 v3, v152, v153
	ds_write_b64 v225, v[2:3] offset:7168
	s_waitcnt vmcnt(16)
	v_cvt_pk_bf16_f32 v2, v154, v155
	v_cvt_pk_bf16_f32 v3, v156, v157
	ds_write_b64 v224, v[2:3] offset:7680
	v_lshlrev_b32_e32 v2, 10, v234
	s_waitcnt lgkmcnt(14)
	v_mfma_f32_16x16x32_bf16 v[130:133], v[122:125], v[138:141], v[106:109]
	v_and_or_b32 v122, v2, s0, v203
	buffer_load_dwordx4 v[2:5], v122, s[4:7], 0 offen nt
	v_or_b32_e32 v10, 0x2000, v122
	v_mfma_f32_16x16x32_bf16 v[134:137], v[134:137], v[138:141], v[114:117]
	v_or_b32_e32 v14, 0x4000, v122
	v_or_b32_e32 v22, 0x6000, v122
	v_or_b32_e32 v30, 0x8000, v122
	v_or_b32_e32 v38, 0xa000, v122
	v_or_b32_e32 v46, 0xc000, v122
	v_or_b32_e32 v54, 0xe000, v122
	v_or_b32_e32 v62, 0x10000, v122
	v_or_b32_e32 v70, 0x12000, v122
	v_or_b32_e32 v78, 0x14000, v122
	v_or_b32_e32 v86, 0x16000, v122
	v_or_b32_e32 v94, 0x18000, v122
	v_or_b32_e32 v106, 0x1a000, v122
	v_or_b32_e32 v114, 0x1c000, v122
	v_or_b32_e32 v122, 0x1e000, v122
	buffer_load_dwordx4 v[54:57], v54, s[4:7], 0 offen nt
	s_nop 0
	buffer_load_dwordx4 v[62:65], v62, s[4:7], 0 offen nt
	s_nop 0
	buffer_load_dwordx4 v[70:73], v70, s[4:7], 0 offen nt
	s_nop 0
	buffer_load_dwordx4 v[78:81], v78, s[4:7], 0 offen nt
	s_nop 0
	buffer_load_dwordx4 v[86:89], v86, s[4:7], 0 offen nt
	s_nop 0
	buffer_load_dwordx4 v[94:97], v94, s[4:7], 0 offen nt
	s_nop 0
	buffer_load_dwordx4 v[106:109], v106, s[4:7], 0 offen nt
	s_nop 0
	buffer_load_dwordx4 v[114:117], v114, s[4:7], 0 offen nt
	s_nop 0
	buffer_load_dwordx4 v[122:125], v122, s[4:7], 0 offen nt
	s_nop 0
	buffer_load_dwordx4 v[10:13], v10, s[4:7], 0 offen nt
	s_nop 0
	buffer_load_dwordx4 v[14:17], v14, s[4:7], 0 offen nt
	s_nop 0
	buffer_load_dwordx4 v[22:25], v22, s[4:7], 0 offen nt
	s_nop 0
	buffer_load_dwordx4 v[30:33], v30, s[4:7], 0 offen nt
	s_nop 0
	buffer_load_dwordx4 v[38:41], v38, s[4:7], 0 offen nt
	s_nop 0
	buffer_load_dwordx4 v[46:49], v46, s[4:7], 0 offen nt
	v_lshlrev_b32_e32 v138, 3, v235
	v_and_b32_e32 v150, 56, v138
	v_lshl_or_b32 v138, v150, 10, v198
	ds_read_b128 v[138:141], v138
	v_lshl_or_b32 v142, v150, 8, v204
	ds_read_b128 v[142:145], v142
	ds_read_b128 v[146:149], v223
	s_waitcnt vmcnt(19)
	v_cvt_pk_bf16_f32 v6, v6, v7
	v_cvt_pk_bf16_f32 v7, v8, v9
	s_waitcnt lgkmcnt(0)
	v_mfma_f32_16x16x32_bf16 v[134:137], v[142:145], v[146:149], v[134:137]
	v_or_b32_e32 v142, 1, v150
	v_mfma_f32_16x16x32_bf16 v[130:133], v[138:141], v[146:149], v[130:133]
	v_lshl_or_b32 v138, v142, 10, v198
	ds_read_b128 v[138:141], v138
	v_lshl_or_b32 v142, v142, 8, v204
	ds_read_b128 v[142:145], v142
	ds_read_b128 v[146:149], v222
	s_waitcnt lgkmcnt(0)
	v_mfma_f32_16x16x32_bf16 v[134:137], v[142:145], v[146:149], v[134:137]
	v_or_b32_e32 v142, 2, v150
	v_mfma_f32_16x16x32_bf16 v[130:133], v[138:141], v[146:149], v[130:133]
	v_lshl_or_b32 v138, v142, 10, v198
	ds_read_b128 v[138:141], v138
	v_lshl_or_b32 v142, v142, 8, v204
	ds_read_b128 v[142:145], v142
	ds_read_b128 v[146:149], v221
	s_waitcnt lgkmcnt(0)
	v_mfma_f32_16x16x32_bf16 v[134:137], v[142:145], v[146:149], v[134:137]
	v_or_b32_e32 v142, 3, v150
	v_mfma_f32_16x16x32_bf16 v[130:133], v[138:141], v[146:149], v[130:133]
	v_lshl_or_b32 v138, v142, 10, v198
	ds_read_b128 v[138:141], v138
	v_lshl_or_b32 v142, v142, 8, v204
	ds_read_b128 v[142:145], v142
	ds_read_b128 v[146:149], v219
	s_waitcnt lgkmcnt(0)
	v_mfma_f32_16x16x32_bf16 v[134:137], v[142:145], v[146:149], v[134:137]
	v_or_b32_e32 v142, 4, v150
	v_mfma_f32_16x16x32_bf16 v[130:133], v[138:141], v[146:149], v[130:133]
	v_lshl_or_b32 v138, v142, 10, v198
	ds_read_b128 v[138:141], v138
	v_lshl_or_b32 v142, v142, 8, v204
	ds_read_b128 v[142:145], v142
	ds_read_b128 v[146:149], v218
	s_waitcnt lgkmcnt(0)
	v_mfma_f32_16x16x32_bf16 v[134:137], v[142:145], v[146:149], v[134:137]
	v_or_b32_e32 v142, 5, v150
	v_mfma_f32_16x16x32_bf16 v[130:133], v[138:141], v[146:149], v[130:133]
	v_lshl_or_b32 v138, v142, 10, v198
	ds_read_b128 v[138:141], v138
	v_lshl_or_b32 v142, v142, 8, v204
	ds_read_b128 v[142:145], v142
	ds_read_b128 v[146:149], v217
	s_waitcnt lgkmcnt(0)
	v_mfma_f32_16x16x32_bf16 v[134:137], v[142:145], v[146:149], v[134:137]
	v_or_b32_e32 v142, 6, v150
	v_mfma_f32_16x16x32_bf16 v[130:133], v[138:141], v[146:149], v[130:133]
	v_lshl_or_b32 v138, v142, 10, v198
	ds_read_b128 v[138:141], v138
	v_lshl_or_b32 v142, v142, 8, v204
	ds_read_b128 v[142:145], v142
	ds_read_b128 v[146:149], v216
	s_waitcnt lgkmcnt(0)
	v_mfma_f32_16x16x32_bf16 v[134:137], v[142:145], v[146:149], v[134:137]
	v_or_b32_e32 v142, 7, v150
	v_mfma_f32_16x16x32_bf16 v[130:133], v[138:141], v[146:149], v[130:133]
	v_lshl_or_b32 v138, v142, 10, v198
	v_lshl_or_b32 v142, v142, 8, v204
	ds_read_b128 v[138:141], v138
	ds_read_b128 v[142:145], v142
	ds_read_b128 v[146:149], v213
	ds_write_b64 v212, v[6:7]
	s_waitcnt vmcnt(18)
	v_cvt_pk_bf16_f32 v6, v18, v19
	v_cvt_pk_bf16_f32 v7, v20, v21
	ds_write_b64 v211, v[6:7] offset:512
	s_waitcnt vmcnt(17)
	v_cvt_pk_bf16_f32 v6, v26, v27
	v_cvt_pk_bf16_f32 v7, v28, v29
	ds_write_b64 v210, v[6:7] offset:1024
	s_waitcnt vmcnt(16)
	v_cvt_pk_bf16_f32 v6, v34, v35
	v_cvt_pk_bf16_f32 v7, v36, v37
	ds_write_b64 v209, v[6:7] offset:1536
	v_cvt_pk_bf16_f32 v6, v42, v43
	v_cvt_pk_bf16_f32 v7, v44, v45
	ds_write_b64 v208, v[6:7] offset:2048
	v_cvt_pk_bf16_f32 v6, v50, v51
	v_cvt_pk_bf16_f32 v7, v52, v53
	ds_write_b64 v207, v[6:7] offset:2560
	v_cvt_pk_bf16_f32 v6, v58, v59
	v_cvt_pk_bf16_f32 v7, v60, v61
	ds_write_b64 v206, v[6:7] offset:3072
	v_cvt_pk_bf16_f32 v6, v66, v67
	v_cvt_pk_bf16_f32 v7, v68, v69
	ds_write_b64 v205, v[6:7] offset:3584
	v_cvt_pk_bf16_f32 v6, v74, v75
	v_cvt_pk_bf16_f32 v7, v76, v77
	ds_write_b64 v231, v[6:7] offset:4096
	v_cvt_pk_bf16_f32 v6, v82, v83
	v_cvt_pk_bf16_f32 v7, v84, v85
	ds_write_b64 v230, v[6:7] offset:4608
	v_cvt_pk_bf16_f32 v6, v90, v91
	v_cvt_pk_bf16_f32 v7, v92, v93
	ds_write_b64 v229, v[6:7] offset:5120
	v_cvt_pk_bf16_f32 v6, v98, v99
	v_cvt_pk_bf16_f32 v7, v100, v101
	ds_write_b64 v228, v[6:7] offset:5632
	v_cvt_pk_bf16_f32 v6, v102, v103
	v_cvt_pk_bf16_f32 v7, v104, v105
	ds_write_b64 v227, v[6:7] offset:6144
	v_cvt_pk_bf16_f32 v6, v110, v111
	v_cvt_pk_bf16_f32 v7, v112, v113
	ds_write_b64 v226, v[6:7] offset:6656
	v_cvt_pk_bf16_f32 v6, v118, v119
	v_cvt_pk_bf16_f32 v7, v120, v121
	ds_write_b64 v225, v[6:7] offset:7168
	v_cvt_pk_bf16_f32 v6, v126, v127
	v_cvt_pk_bf16_f32 v7, v128, v129
	ds_write_b64 v224, v[6:7] offset:7680
	v_add_u32_e32 v6, 0x1800, v196
	v_and_or_b32 v126, v6, s0, v203
	buffer_load_dwordx4 v[6:9], v126, s[4:7], 0 offen nt
	v_or_b32_e32 v18, 0x2000, v126
	v_or_b32_e32 v26, 0x4000, v126
	v_or_b32_e32 v34, 0x6000, v126
	v_or_b32_e32 v42, 0x8000, v126
	v_or_b32_e32 v50, 0xa000, v126
	v_or_b32_e32 v58, 0xc000, v126
	v_or_b32_e32 v66, 0xe000, v126
	v_or_b32_e32 v74, 0x10000, v126
	v_or_b32_e32 v82, 0x12000, v126
	v_or_b32_e32 v90, 0x14000, v126
	v_or_b32_e32 v98, 0x16000, v126
	v_or_b32_e32 v102, 0x18000, v126
	v_or_b32_e32 v110, 0x1a000, v126
	v_or_b32_e32 v118, 0x1c000, v126
	v_or_b32_e32 v126, 0x1e000, v126
	buffer_load_dwordx4 v[50:53], v50, s[4:7], 0 offen nt
	s_waitcnt lgkmcnt(14)
	v_mfma_f32_16x16x32_bf16 v[130:133], v[138:141], v[146:149], v[130:133]
	buffer_load_dwordx4 v[58:61], v58, s[4:7], 0 offen nt
	s_nop 0
	buffer_load_dwordx4 v[66:69], v66, s[4:7], 0 offen nt
	v_mfma_f32_16x16x32_bf16 v[134:137], v[142:145], v[146:149], v[134:137]
	buffer_load_dwordx4 v[74:77], v74, s[4:7], 0 offen nt
	v_add_u32_e32 v142, 7, v200
	buffer_load_dwordx4 v[82:85], v82, s[4:7], 0 offen nt
	s_nop 0
	buffer_load_dwordx4 v[90:93], v90, s[4:7], 0 offen nt
	s_nop 0
	buffer_load_dwordx4 v[98:101], v98, s[4:7], 0 offen nt
	s_nop 0
	buffer_load_dwordx4 v[102:105], v102, s[4:7], 0 offen nt
	s_nop 0
	buffer_load_dwordx4 v[110:113], v110, s[4:7], 0 offen nt
	s_nop 0
	buffer_load_dwordx4 v[118:121], v118, s[4:7], 0 offen nt
	s_nop 0
	buffer_load_dwordx4 v[126:129], v126, s[4:7], 0 offen nt
	s_nop 0
	buffer_load_dwordx4 v[18:21], v18, s[4:7], 0 offen nt
	s_nop 0
	buffer_load_dwordx4 v[26:29], v26, s[4:7], 0 offen nt
	s_nop 0
	buffer_load_dwordx4 v[34:37], v34, s[4:7], 0 offen nt
	s_nop 0
	buffer_load_dwordx4 v[42:45], v42, s[4:7], 0 offen nt
	v_xor_b32_e32 v143, 32, v232
	v_lshl_or_b32 v138, v143, 10, v198
	ds_read_b128 v[138:141], v138
	v_lshl_or_b32 v143, v143, 8, v204
	ds_read_b128 v[144:147], v143
	ds_read_b128 v[148:151], v223
	v_bitop3_b32 v143, v232, 1, 32 bitop3:0xde
	s_waitcnt vmcnt(31)
	v_cvt_pk_bf16_f32 v2, v2, v3
	s_waitcnt lgkmcnt(0)
	v_mfma_f32_16x16x32_bf16 v[134:137], v[144:147], v[148:151], v[134:137]
	v_cvt_pk_bf16_f32 v3, v4, v5
	v_mfma_f32_16x16x32_bf16 v[130:133], v[138:141], v[148:151], v[130:133]
	v_lshl_or_b32 v138, v143, 10, v198
	ds_read_b128 v[138:141], v138
	v_lshl_or_b32 v143, v143, 8, v204
	ds_read_b128 v[144:147], v143
	ds_read_b128 v[148:151], v222
	v_bitop3_b32 v143, v232, 2, 32 bitop3:0xde
	s_waitcnt lgkmcnt(0)
	v_mfma_f32_16x16x32_bf16 v[134:137], v[144:147], v[148:151], v[134:137]
	v_mfma_f32_16x16x32_bf16 v[130:133], v[138:141], v[148:151], v[130:133]
	v_lshl_or_b32 v138, v143, 10, v198
	ds_read_b128 v[138:141], v138
	v_lshl_or_b32 v143, v143, 8, v204
	ds_read_b128 v[144:147], v143
	ds_read_b128 v[148:151], v221
	v_bitop3_b32 v143, v232, 3, 32 bitop3:0xde
	s_waitcnt lgkmcnt(0)
	v_mfma_f32_16x16x32_bf16 v[130:133], v[138:141], v[148:151], v[130:133]
	v_lshl_or_b32 v138, v143, 10, v198
	ds_read_b128 v[138:141], v138
	v_lshl_or_b32 v143, v143, 8, v204
	v_mfma_f32_16x16x32_bf16 v[134:137], v[144:147], v[148:151], v[134:137]
	ds_read_b128 v[144:147], v143
	ds_read_b128 v[148:151], v219
	v_bitop3_b32 v143, v232, 4, 32 bitop3:0xde
	s_waitcnt lgkmcnt(0)
	v_mfma_f32_16x16x32_bf16 v[130:133], v[138:141], v[148:151], v[130:133]
	v_lshl_or_b32 v138, v143, 10, v198
	ds_read_b128 v[138:141], v138
	v_lshl_or_b32 v143, v143, 8, v204
	v_mfma_f32_16x16x32_bf16 v[134:137], v[144:147], v[148:151], v[134:137]
	ds_read_b128 v[144:147], v143
	ds_read_b128 v[148:151], v218
	v_bitop3_b32 v143, v232, 5, 32 bitop3:0xde
	s_waitcnt lgkmcnt(0)
	v_mfma_f32_16x16x32_bf16 v[130:133], v[138:141], v[148:151], v[130:133]
	v_lshl_or_b32 v138, v143, 10, v198
	ds_read_b128 v[138:141], v138
	v_lshl_or_b32 v143, v143, 8, v204
	v_mfma_f32_16x16x32_bf16 v[134:137], v[144:147], v[148:151], v[134:137]
	ds_read_b128 v[144:147], v143
	ds_read_b128 v[148:151], v217
	v_bitop3_b32 v143, v232, 6, 32 bitop3:0xde
	s_waitcnt lgkmcnt(0)
	v_mfma_f32_16x16x32_bf16 v[130:133], v[138:141], v[148:151], v[130:133]
	v_lshl_or_b32 v138, v143, 10, v198
	ds_read_b128 v[138:141], v138
	v_lshl_or_b32 v143, v143, 8, v204
	v_mfma_f32_16x16x32_bf16 v[134:137], v[144:147], v[148:151], v[134:137]
	ds_read_b128 v[144:147], v143
	ds_read_b128 v[148:151], v216
	v_bitop3_b32 v143, v232, 7, 32 bitop3:0xde
	s_waitcnt lgkmcnt(0)
	v_mfma_f32_16x16x32_bf16 v[130:133], v[138:141], v[148:151], v[130:133]
	v_lshl_or_b32 v138, v143, 10, v198
	v_lshl_or_b32 v143, v143, 8, v204
	ds_read_b128 v[138:141], v138
	v_mfma_f32_16x16x32_bf16 v[134:137], v[144:147], v[148:151], v[134:137]
	ds_read_b128 v[144:147], v143
	ds_read_b128 v[148:151], v213
	ds_write_b64 v212, v[2:3]
	s_waitcnt vmcnt(21)
	v_cvt_pk_bf16_f32 v2, v10, v11
	v_cvt_pk_bf16_f32 v3, v12, v13
	ds_write_b64 v211, v[2:3] offset:512
	s_waitcnt vmcnt(20)
	v_cvt_pk_bf16_f32 v2, v14, v15
	v_cvt_pk_bf16_f32 v3, v16, v17
	ds_write_b64 v210, v[2:3] offset:1024
	s_waitcnt vmcnt(19)
	v_cvt_pk_bf16_f32 v2, v22, v23
	v_cvt_pk_bf16_f32 v3, v24, v25
	ds_write_b64 v209, v[2:3] offset:1536
	s_waitcnt vmcnt(18)
	v_cvt_pk_bf16_f32 v2, v30, v31
	v_cvt_pk_bf16_f32 v3, v32, v33
	ds_write_b64 v208, v[2:3] offset:2048
	s_waitcnt vmcnt(17)
	v_cvt_pk_bf16_f32 v2, v38, v39
	v_cvt_pk_bf16_f32 v3, v40, v41
	ds_write_b64 v207, v[2:3] offset:2560
	s_waitcnt vmcnt(16)
	v_cvt_pk_bf16_f32 v2, v46, v47
	v_cvt_pk_bf16_f32 v3, v48, v49
	ds_write_b64 v206, v[2:3] offset:3072
	v_cvt_pk_bf16_f32 v2, v54, v55
	v_cvt_pk_bf16_f32 v3, v56, v57
	ds_write_b64 v205, v[2:3] offset:3584
	v_cvt_pk_bf16_f32 v2, v62, v63
	v_cvt_pk_bf16_f32 v3, v64, v65
	ds_write_b64 v231, v[2:3] offset:4096
	v_cvt_pk_bf16_f32 v2, v70, v71
	v_cvt_pk_bf16_f32 v3, v72, v73
	ds_write_b64 v230, v[2:3] offset:4608
	v_cvt_pk_bf16_f32 v2, v78, v79
	v_cvt_pk_bf16_f32 v3, v80, v81
	ds_write_b64 v229, v[2:3] offset:5120
	v_cvt_pk_bf16_f32 v2, v86, v87
	v_cvt_pk_bf16_f32 v3, v88, v89
	ds_write_b64 v228, v[2:3] offset:5632
	v_cvt_pk_bf16_f32 v2, v94, v95
	v_cvt_pk_bf16_f32 v3, v96, v97
	ds_write_b64 v227, v[2:3] offset:6144
	v_cvt_pk_bf16_f32 v2, v106, v107
	v_cvt_pk_bf16_f32 v3, v108, v109
	ds_write_b64 v226, v[2:3] offset:6656
	v_cvt_pk_bf16_f32 v2, v114, v115
	v_cvt_pk_bf16_f32 v3, v116, v117
	ds_write_b64 v225, v[2:3] offset:7168
	v_cvt_pk_bf16_f32 v2, v122, v123
	v_cvt_pk_bf16_f32 v3, v124, v125
	ds_write_b64 v224, v[2:3] offset:7680
	v_lshlrev_b32_e32 v2, 10, v142
	v_and_or_b32 v2, v2, s0, v203
	v_or_b32_e32 v3, 0x2000, v2
	buffer_load_dwordx4 v[10:13], v2, s[4:7], 0 offen nt
	buffer_load_dwordx4 v[14:17], v3, s[4:7], 0 offen nt
	v_or_b32_e32 v3, 0x4000, v2
	buffer_load_dwordx4 v[22:25], v3, s[4:7], 0 offen nt
	v_or_b32_e32 v3, 0x6000, v2
	buffer_load_dwordx4 v[30:33], v3, s[4:7], 0 offen nt
	v_or_b32_e32 v3, 0x8000, v2
	buffer_load_dwordx4 v[38:41], v3, s[4:7], 0 offen nt
	v_or_b32_e32 v3, 0xa000, v2
	buffer_load_dwordx4 v[46:49], v3, s[4:7], 0 offen nt
	v_or_b32_e32 v3, 0xc000, v2
	buffer_load_dwordx4 v[54:57], v3, s[4:7], 0 offen nt
	v_or_b32_e32 v3, 0xe000, v2
	buffer_load_dwordx4 v[62:65], v3, s[4:7], 0 offen nt
	v_or_b32_e32 v3, 0x10000, v2
	buffer_load_dwordx4 v[70:73], v3, s[4:7], 0 offen nt
	v_or_b32_e32 v3, 0x12000, v2
	buffer_load_dwordx4 v[78:81], v3, s[4:7], 0 offen nt
	v_or_b32_e32 v3, 0x14000, v2
	buffer_load_dwordx4 v[86:89], v3, s[4:7], 0 offen nt
	v_or_b32_e32 v3, 0x16000, v2
	buffer_load_dwordx4 v[94:97], v3, s[4:7], 0 offen nt
	v_or_b32_e32 v3, 0x18000, v2
	buffer_load_dwordx4 v[106:109], v3, s[4:7], 0 offen nt
	v_or_b32_e32 v3, 0x1a000, v2
	buffer_load_dwordx4 v[114:117], v3, s[4:7], 0 offen nt
	v_or_b32_e32 v3, 0x1c000, v2
	v_or_b32_e32 v2, 0x1e000, v2
	s_waitcnt lgkmcnt(14)
	v_mfma_f32_16x16x32_bf16 v[138:141], v[138:141], v[148:151], v[130:133]
	buffer_load_dwordx4 v[122:125], v3, s[4:7], 0 offen nt
	s_nop 1
	buffer_load_dwordx4 v[130:133], v2, s[4:7], 0 offen nt
	v_mfma_f32_16x16x32_bf16 v[134:137], v[144:147], v[148:151], v[134:137]
	v_lshlrev_b32_e32 v2, 3, v234
	v_and_b32_e32 v143, 56, v2
	v_lshl_or_b32 v2, v143, 10, v198
	v_lshl_or_b32 v152, v143, 8, v204
	ds_read_b128 v[2:5], v2
	ds_read_b128 v[144:147], v223
	ds_read_b128 v[148:151], v222
	ds_read_b128 v[152:155], v152
	v_or_b32_e32 v156, 1, v143
	v_lshl_or_b32 v157, v156, 10, v198
	s_waitcnt lgkmcnt(2)
	v_mfma_f32_16x16x32_bf16 v[2:5], v[2:5], v[144:147], v[138:141]
	s_waitcnt vmcnt(31)
	v_cvt_pk_bf16_f32 v6, v6, v7
	v_cvt_pk_bf16_f32 v7, v8, v9
	s_waitcnt lgkmcnt(0)
	v_mfma_f32_16x16x32_bf16 v[134:137], v[152:155], v[144:147], v[134:137]
	ds_read_b128 v[138:141], v157
	v_lshl_or_b32 v144, v156, 8, v204
	ds_read_b128 v[144:147], v144
	v_or_b32_e32 v156, 2, v143
	s_waitcnt lgkmcnt(1)
	v_mfma_f32_16x16x32_bf16 v[2:5], v[138:141], v[148:151], v[2:5]
	v_lshl_or_b32 v138, v156, 10, v198
	ds_read_b128 v[138:141], v138
	ds_read_b128 v[152:155], v221
	s_waitcnt lgkmcnt(2)
	v_mfma_f32_16x16x32_bf16 v[134:137], v[144:147], v[148:151], v[134:137]
	v_lshl_or_b32 v144, v156, 8, v204
	v_or_b32_e32 v156, 3, v143
	ds_read_b128 v[144:147], v144
	ds_read_b128 v[148:151], v219
	s_waitcnt lgkmcnt(2)
	v_mfma_f32_16x16x32_bf16 v[2:5], v[138:141], v[152:155], v[2:5]
	v_lshl_or_b32 v138, v156, 10, v198
	ds_read_b128 v[138:141], v138
	s_waitcnt lgkmcnt(2)
	v_mfma_f32_16x16x32_bf16 v[134:137], v[144:147], v[152:155], v[134:137]
	v_lshl_or_b32 v144, v156, 8, v204
	ds_read_b128 v[144:147], v144
	v_or_b32_e32 v152, 4, v143
	s_waitcnt lgkmcnt(1)
	v_mfma_f32_16x16x32_bf16 v[2:5], v[138:141], v[148:151], v[2:5]
	v_lshl_or_b32 v138, v152, 10, v198
	ds_read_b128 v[138:141], v138
	v_or_b32_e32 v156, 5, v143
	s_waitcnt lgkmcnt(1)
	v_mfma_f32_16x16x32_bf16 v[134:137], v[144:147], v[148:151], v[134:137]
	ds_read_b128 v[144:147], v218
	v_lshl_or_b32 v148, v152, 8, v204
	ds_read_b128 v[148:151], v148
	ds_read_b128 v[152:155], v217
	s_waitcnt lgkmcnt(2)
	v_mfma_f32_16x16x32_bf16 v[2:5], v[138:141], v[144:147], v[2:5]
	v_lshl_or_b32 v138, v156, 10, v198
	ds_read_b128 v[138:141], v138
	s_waitcnt lgkmcnt(2)
	v_mfma_f32_16x16x32_bf16 v[134:137], v[148:151], v[144:147], v[134:137]
	v_lshl_or_b32 v144, v156, 8, v204
	ds_read_b128 v[144:147], v144
	v_or_b32_e32 v148, 6, v143
	s_waitcnt lgkmcnt(1)
	v_mfma_f32_16x16x32_bf16 v[2:5], v[138:141], v[152:155], v[2:5]
	v_lshl_or_b32 v138, v148, 10, v198
	ds_read_b128 v[138:141], v138
	v_lshl_or_b32 v148, v148, 8, v204
	s_waitcnt lgkmcnt(1)
	v_mfma_f32_16x16x32_bf16 v[134:137], v[144:147], v[152:155], v[134:137]
	ds_read_b128 v[144:147], v216
	ds_read_b128 v[148:151], v148
	ds_read_b128 v[152:155], v213
	v_or_b32_e32 v143, 7, v143
	ds_write_b64 v212, v[6:7]
	s_waitcnt lgkmcnt(3)
	v_mfma_f32_16x16x32_bf16 v[2:5], v[138:141], v[144:147], v[2:5]
	v_lshl_or_b32 v138, v143, 10, v198
	v_lshl_or_b32 v143, v143, 8, v204
	s_waitcnt vmcnt(19)
	v_cvt_pk_bf16_f32 v6, v18, v19
	v_cvt_pk_bf16_f32 v7, v20, v21
	ds_read_b128 v[138:141], v138
	s_waitcnt lgkmcnt(3)
	v_mfma_f32_16x16x32_bf16 v[134:137], v[148:151], v[144:147], v[134:137]
	ds_read_b128 v[144:147], v143
	ds_write_b64 v211, v[6:7] offset:512
	s_waitcnt vmcnt(18)
	v_cvt_pk_bf16_f32 v6, v26, v27
	v_cvt_pk_bf16_f32 v7, v28, v29
	ds_write_b64 v210, v[6:7] offset:1024
	s_waitcnt vmcnt(17)
	v_cvt_pk_bf16_f32 v6, v34, v35
	v_cvt_pk_bf16_f32 v7, v36, v37
	ds_write_b64 v209, v[6:7] offset:1536
	s_waitcnt vmcnt(16)
	v_cvt_pk_bf16_f32 v6, v42, v43
	v_cvt_pk_bf16_f32 v7, v44, v45
	ds_write_b64 v208, v[6:7] offset:2048
	v_cvt_pk_bf16_f32 v6, v50, v51
	v_cvt_pk_bf16_f32 v7, v52, v53
	ds_write_b64 v207, v[6:7] offset:2560
	v_cvt_pk_bf16_f32 v6, v58, v59
	v_cvt_pk_bf16_f32 v7, v60, v61
	ds_write_b64 v206, v[6:7] offset:3072
	v_cvt_pk_bf16_f32 v6, v66, v67
	v_cvt_pk_bf16_f32 v7, v68, v69
	ds_write_b64 v205, v[6:7] offset:3584
	v_cvt_pk_bf16_f32 v6, v74, v75
	v_cvt_pk_bf16_f32 v7, v76, v77
	ds_write_b64 v231, v[6:7] offset:4096
	v_cvt_pk_bf16_f32 v6, v82, v83
	v_cvt_pk_bf16_f32 v7, v84, v85
	ds_write_b64 v230, v[6:7] offset:4608
	v_cvt_pk_bf16_f32 v6, v90, v91
	v_cvt_pk_bf16_f32 v7, v92, v93
	s_waitcnt lgkmcnt(9)
	v_mfma_f32_16x16x32_bf16 v[134:137], v[144:147], v[152:155], v[134:137]
	ds_write_b64 v229, v[6:7] offset:5120
	v_cvt_pk_bf16_f32 v6, v98, v99
	v_cvt_pk_bf16_f32 v7, v100, v101
	ds_write_b64 v228, v[6:7] offset:5632
	v_cvt_pk_bf16_f32 v6, v102, v103
	v_cvt_pk_bf16_f32 v7, v104, v105
	ds_write_b64 v227, v[6:7] offset:6144
	v_cvt_pk_bf16_f32 v6, v110, v111
	v_cvt_pk_bf16_f32 v7, v112, v113
	ds_write_b64 v226, v[6:7] offset:6656
	v_cvt_pk_bf16_f32 v6, v118, v119
	v_cvt_pk_bf16_f32 v7, v120, v121
	v_mfma_f32_16x16x32_bf16 v[2:5], v[138:141], v[152:155], v[2:5]
	ds_write_b64 v225, v[6:7] offset:7168
	v_cvt_pk_bf16_f32 v6, v126, v127
	v_cvt_pk_bf16_f32 v7, v128, v129
	ds_write_b64 v224, v[6:7] offset:7680
	v_add_u32_e32 v6, 48, v232
	v_and_b32_e32 v50, 56, v6
	v_lshl_or_b32 v6, v50, 10, v198
	v_lshl_or_b32 v34, v50, 8, v204
	ds_read_b128 v[6:9], v6
	ds_read_b128 v[18:21], v223
	ds_read_b128 v[26:29], v222
	ds_read_b128 v[34:37], v34
	v_or_b32_e32 v42, 1, v50
	v_lshl_or_b32 v43, v42, 10, v198
	s_waitcnt lgkmcnt(2)
	v_mfma_f32_16x16x32_bf16 v[2:5], v[6:9], v[18:21], v[2:5]
	ds_read_b128 v[6:9], v43
	v_or_b32_e32 v51, 2, v50
	s_waitcnt lgkmcnt(1)
	v_mfma_f32_16x16x32_bf16 v[18:21], v[34:37], v[18:21], v[134:137]
	v_lshl_or_b32 v34, v42, 8, v204
	ds_read_b128 v[34:37], v34
	s_waitcnt lgkmcnt(1)
	v_mfma_f32_16x16x32_bf16 v[2:5], v[6:9], v[26:29], v[2:5]
	v_lshl_or_b32 v6, v51, 10, v198
	ds_read_b128 v[6:9], v6
	ds_read_b128 v[42:45], v221
	s_waitcnt lgkmcnt(2)
	v_mfma_f32_16x16x32_bf16 v[18:21], v[34:37], v[26:29], v[18:21]
	v_lshl_or_b32 v26, v51, 8, v204
	v_or_b32_e32 v51, 3, v50
	ds_read_b128 v[26:29], v26
	ds_read_b128 v[34:37], v219
	s_waitcnt lgkmcnt(2)
	v_mfma_f32_16x16x32_bf16 v[2:5], v[6:9], v[42:45], v[2:5]
	v_lshl_or_b32 v6, v51, 10, v198
	ds_read_b128 v[6:9], v6
	s_waitcnt lgkmcnt(2)
	v_mfma_f32_16x16x32_bf16 v[18:21], v[26:29], v[42:45], v[18:21]
	v_lshl_or_b32 v26, v51, 8, v204
	ds_read_b128 v[26:29], v26
	v_or_b32_e32 v42, 4, v50
	s_waitcnt lgkmcnt(1)
	v_mfma_f32_16x16x32_bf16 v[2:5], v[6:9], v[34:37], v[2:5]
	v_lshl_or_b32 v6, v42, 10, v198
	ds_read_b128 v[6:9], v6
	v_or_b32_e32 v51, 5, v50
	s_waitcnt lgkmcnt(1)
	v_mfma_f32_16x16x32_bf16 v[18:21], v[26:29], v[34:37], v[18:21]
	ds_read_b128 v[26:29], v218
	v_lshl_or_b32 v34, v42, 8, v204
	ds_read_b128 v[34:37], v34
	ds_read_b128 v[42:45], v217
	s_waitcnt lgkmcnt(2)
	v_mfma_f32_16x16x32_bf16 v[2:5], v[6:9], v[26:29], v[2:5]
	v_lshl_or_b32 v6, v51, 10, v198
	ds_read_b128 v[6:9], v6
	s_waitcnt lgkmcnt(2)
	v_mfma_f32_16x16x32_bf16 v[18:21], v[34:37], v[26:29], v[18:21]
	v_lshl_or_b32 v26, v51, 8, v204
	ds_read_b128 v[26:29], v26
	v_or_b32_e32 v34, 6, v50
	s_waitcnt lgkmcnt(1)
	v_mfma_f32_16x16x32_bf16 v[2:5], v[6:9], v[42:45], v[2:5]
	v_lshl_or_b32 v6, v34, 10, v198
	ds_read_b128 v[6:9], v6
	v_lshl_or_b32 v34, v34, 8, v204
	s_waitcnt lgkmcnt(1)
	v_mfma_f32_16x16x32_bf16 v[18:21], v[26:29], v[42:45], v[18:21]
	ds_read_b128 v[26:29], v216
	ds_read_b128 v[34:37], v34
	ds_read_b128 v[42:45], v213
	v_or_b32_e32 v50, 7, v50
	s_waitcnt lgkmcnt(2)
	v_mfma_f32_16x16x32_bf16 v[2:5], v[6:9], v[26:29], v[2:5]
	v_lshl_or_b32 v6, v50, 10, v198
	ds_read_b128 v[6:9], v6
	s_waitcnt lgkmcnt(2)
	v_mfma_f32_16x16x32_bf16 v[18:21], v[34:37], v[26:29], v[18:21]
	v_lshl_or_b32 v26, v50, 8, v204
	ds_read_b128 v[26:29], v26
	s_waitcnt lgkmcnt(1)
	v_mfma_f32_16x16x32_bf16 v[34:37], v[6:9], v[42:45], v[2:5]
	v_and_b32_e32 v74, 7, v197
	v_lshrrev_b32_e32 v75, 3, v197
	v_lshlrev_b32_e32 v192, 13, v200
	v_lshlrev_b32_e32 v193, 11, v200
	v_lshl_add_u32 v203, v197, 2, v196
	v_lshl_or_b32 v192, v75, 8, v192
	v_lshl_or_b32 v193, v75, 6, v193
	v_add_u32_e32 v203, 0x24800, v203
	v_lshl_or_b32 v192, v201, 6, v192
	v_lshl_or_b32 v193, v74, 1, v193
	v_lshl_or_b32 v192, v74, 1, v192
	v_or_b32_e32 v193, 0x10000, v193
	v_cmp_gt_u32_e64 s[36:37], 16, v1
	v_cmp_eq_u32_e64 s[38:39], 1, v201
	ds_read2_b32 v[2:3], v203 offset1:16
	ds_read2_b32 v[4:5], v203 offset0:32 offset1:48
	ds_read2_b32 v[6:7], v203 offset0:64 offset1:80
	ds_read2_b32 v[8:9], v203 offset0:96 offset1:112
	ds_read2_b32 v[50:51], v203 offset0:128 offset1:144
	ds_read2_b32 v[52:53], v203 offset0:160 offset1:176
	ds_read2_b32 v[58:59], v203 offset0:192 offset1:208
	ds_read2_b32 v[60:61], v203 offset0:224 offset1:240
	v_mov_b32_e32 v146, 0
	v_mov_b32_e32 v147, 0
	v_mov_b32_e32 v150, 0
	v_mov_b32_e32 v151, 0
	v_mov_b32_e32 v154, 0
	v_mov_b32_e32 v155, 0
	v_mov_b32_e32 v158, 0
	v_mov_b32_e32 v159, 0
	v_mov_b32_e32 v162, 0
	v_mov_b32_e32 v163, 0
	v_mov_b32_e32 v166, 0
	v_mov_b32_e32 v167, 0
	v_mov_b32_e32 v170, 0
	v_mov_b32_e32 v171, 0
	v_mov_b32_e32 v174, 0
	v_mov_b32_e32 v175, 0
	v_mov_b32_e32 v178, 0
	v_mov_b32_e32 v179, 0
	v_mov_b32_e32 v182, 0
	v_mov_b32_e32 v183, 0
	v_mov_b32_e32 v186, 0
	v_mov_b32_e32 v187, 0
	v_mov_b32_e32 v190, 0
	v_mov_b32_e32 v191, 0
	v_mov_b32_e32 v234, 0
	v_mov_b32_e32 v235, 0
	v_mov_b32_e32 v238, 0
	v_mov_b32_e32 v239, 0
	v_mov_b32_e32 v242, 0
	v_mov_b32_e32 v243, 0
	v_mov_b32_e32 v246, 0
	v_mov_b32_e32 v247, 0
	ds_read_u16 v82, v192
	ds_read_u16 v83, v192 offset:16
	ds_read_u16 v84, v192 offset:32
	ds_read_u16 v85, v192 offset:48
	ds_read_u16 v90, v193
	ds_read_u16 v91, v193 offset:16
	ds_read_u16 v92, v193 offset:32
	ds_read_u16 v93, v193 offset:48
	ds_read_u16 v98, v192 offset:512
	ds_read_u16 v99, v192 offset:528
	ds_read_u16 v100, v192 offset:544
	ds_read_u16 v101, v192 offset:560
	ds_read_u16 v102, v193 offset:128
	ds_read_u16 v103, v193 offset:144
	ds_read_u16 v104, v193 offset:160
	ds_read_u16 v105, v193 offset:176
	s_waitcnt lgkmcnt(8)
	v_lshl_or_b32 v144, v83, 16, v82
	v_lshl_or_b32 v145, v85, 16, v84
	s_mov_b64 exec, s[36:37]
	v_lshl_or_b32 v146, v91, 16, v90
	v_lshl_or_b32 v147, v93, 16, v92
	s_mov_b64 exec, -1
	ds_read_u16 v82, v192 offset:1024
	ds_read_u16 v83, v192 offset:1040
	ds_read_u16 v84, v192 offset:1056
	ds_read_u16 v85, v192 offset:1072
	ds_read_u16 v90, v193 offset:256
	ds_read_u16 v91, v193 offset:272
	ds_read_u16 v92, v193 offset:288
	ds_read_u16 v93, v193 offset:304
	s_waitcnt lgkmcnt(8)
	v_lshl_or_b32 v148, v99, 16, v98
	v_lshl_or_b32 v149, v101, 16, v100
	s_mov_b64 exec, s[36:37]
	v_lshl_or_b32 v150, v103, 16, v102
	v_lshl_or_b32 v151, v105, 16, v104
	s_mov_b64 exec, -1
	ds_read_u16 v98, v192 offset:1536
	ds_read_u16 v99, v192 offset:1552
	ds_read_u16 v100, v192 offset:1568
	ds_read_u16 v101, v192 offset:1584
	ds_read_u16 v102, v193 offset:384
	ds_read_u16 v103, v193 offset:400
	ds_read_u16 v104, v193 offset:416
	ds_read_u16 v105, v193 offset:432
	s_waitcnt lgkmcnt(8)
	v_lshl_or_b32 v152, v83, 16, v82
	v_lshl_or_b32 v153, v85, 16, v84
	s_mov_b64 exec, s[36:37]
	v_lshl_or_b32 v154, v91, 16, v90
	v_lshl_or_b32 v155, v93, 16, v92
	s_mov_b64 exec, -1
	ds_read_u16 v82, v192 offset:2048
	ds_read_u16 v83, v192 offset:2064
	ds_read_u16 v84, v192 offset:2080
	ds_read_u16 v85, v192 offset:2096
	ds_read_u16 v90, v193 offset:512
	ds_read_u16 v91, v193 offset:528
	ds_read_u16 v92, v193 offset:544
	ds_read_u16 v93, v193 offset:560
	s_waitcnt lgkmcnt(8)
	v_lshl_or_b32 v156, v99, 16, v98
	v_lshl_or_b32 v157, v101, 16, v100
	s_mov_b64 exec, s[36:37]
	v_lshl_or_b32 v158, v103, 16, v102
	v_lshl_or_b32 v159, v105, 16, v104
	s_mov_b64 exec, -1
	ds_read_u16 v98, v192 offset:2560
	ds_read_u16 v99, v192 offset:2576
	ds_read_u16 v100, v192 offset:2592
	ds_read_u16 v101, v192 offset:2608
	ds_read_u16 v102, v193 offset:640
	ds_read_u16 v103, v193 offset:656
	ds_read_u16 v104, v193 offset:672
	ds_read_u16 v105, v193 offset:688
	s_waitcnt lgkmcnt(8)
	v_lshl_or_b32 v160, v83, 16, v82
	v_lshl_or_b32 v161, v85, 16, v84
	s_mov_b64 exec, s[36:37]
	v_lshl_or_b32 v162, v91, 16, v90
	v_lshl_or_b32 v163, v93, 16, v92
	s_mov_b64 exec, -1
	ds_read_u16 v82, v192 offset:3072
	ds_read_u16 v83, v192 offset:3088
	ds_read_u16 v84, v192 offset:3104
	ds_read_u16 v85, v192 offset:3120
	ds_read_u16 v90, v193 offset:768
	ds_read_u16 v91, v193 offset:784
	ds_read_u16 v92, v193 offset:800
	ds_read_u16 v93, v193 offset:816
	s_waitcnt lgkmcnt(8)
	v_lshl_or_b32 v164, v99, 16, v98
	v_lshl_or_b32 v165, v101, 16, v100
	s_mov_b64 exec, s[36:37]
	v_lshl_or_b32 v166, v103, 16, v102
	v_lshl_or_b32 v167, v105, 16, v104
	s_mov_b64 exec, -1
	ds_read_u16 v98, v192 offset:3584
	ds_read_u16 v99, v192 offset:3600
	ds_read_u16 v100, v192 offset:3616
	ds_read_u16 v101, v192 offset:3632
	ds_read_u16 v102, v193 offset:896
	ds_read_u16 v103, v193 offset:912
	ds_read_u16 v104, v193 offset:928
	ds_read_u16 v105, v193 offset:944
	s_waitcnt lgkmcnt(8)
	v_lshl_or_b32 v168, v83, 16, v82
	v_lshl_or_b32 v169, v85, 16, v84
	s_mov_b64 exec, s[36:37]
	v_lshl_or_b32 v170, v91, 16, v90
	v_lshl_or_b32 v171, v93, 16, v92
	s_mov_b64 exec, -1
	ds_read_u16 v82, v192 offset:4096
	ds_read_u16 v83, v192 offset:4112
	ds_read_u16 v84, v192 offset:4128
	ds_read_u16 v85, v192 offset:4144
	ds_read_u16 v90, v193 offset:1024
	ds_read_u16 v91, v193 offset:1040
	ds_read_u16 v92, v193 offset:1056
	ds_read_u16 v93, v193 offset:1072
	s_waitcnt lgkmcnt(8)
	v_lshl_or_b32 v172, v99, 16, v98
	v_lshl_or_b32 v173, v101, 16, v100
	s_mov_b64 exec, s[36:37]
	v_lshl_or_b32 v174, v103, 16, v102
	v_lshl_or_b32 v175, v105, 16, v104
	s_mov_b64 exec, -1
	ds_read_u16 v98, v192 offset:4608
	ds_read_u16 v99, v192 offset:4624
	ds_read_u16 v100, v192 offset:4640
	ds_read_u16 v101, v192 offset:4656
	ds_read_u16 v102, v193 offset:1152
	ds_read_u16 v103, v193 offset:1168
	ds_read_u16 v104, v193 offset:1184
	ds_read_u16 v105, v193 offset:1200
	s_waitcnt lgkmcnt(8)
	v_lshl_or_b32 v176, v83, 16, v82
	v_lshl_or_b32 v177, v85, 16, v84
	s_mov_b64 exec, s[36:37]
	v_lshl_or_b32 v178, v91, 16, v90
	v_lshl_or_b32 v179, v93, 16, v92
	s_mov_b64 exec, -1
	ds_read_u16 v82, v192 offset:5120
	ds_read_u16 v83, v192 offset:5136
	ds_read_u16 v84, v192 offset:5152
	ds_read_u16 v85, v192 offset:5168
	ds_read_u16 v90, v193 offset:1280
	ds_read_u16 v91, v193 offset:1296
	ds_read_u16 v92, v193 offset:1312
	ds_read_u16 v93, v193 offset:1328
	s_waitcnt lgkmcnt(8)
	v_lshl_or_b32 v180, v99, 16, v98
	v_lshl_or_b32 v181, v101, 16, v100
	s_mov_b64 exec, s[36:37]
	v_lshl_or_b32 v182, v103, 16, v102
	v_lshl_or_b32 v183, v105, 16, v104
	s_mov_b64 exec, -1
	ds_read_u16 v98, v192 offset:5632
	ds_read_u16 v99, v192 offset:5648
	ds_read_u16 v100, v192 offset:5664
	ds_read_u16 v101, v192 offset:5680
	ds_read_u16 v102, v193 offset:1408
	ds_read_u16 v103, v193 offset:1424
	ds_read_u16 v104, v193 offset:1440
	ds_read_u16 v105, v193 offset:1456
	s_waitcnt lgkmcnt(8)
	v_lshl_or_b32 v184, v83, 16, v82
	v_lshl_or_b32 v185, v85, 16, v84
	s_mov_b64 exec, s[36:37]
	v_lshl_or_b32 v186, v91, 16, v90
	v_lshl_or_b32 v187, v93, 16, v92
	s_mov_b64 exec, -1
	ds_read_u16 v82, v192 offset:6144
	ds_read_u16 v83, v192 offset:6160
	ds_read_u16 v84, v192 offset:6176
	ds_read_u16 v85, v192 offset:6192
	ds_read_u16 v90, v193 offset:1536
	ds_read_u16 v91, v193 offset:1552
	ds_read_u16 v92, v193 offset:1568
	ds_read_u16 v93, v193 offset:1584
	s_waitcnt lgkmcnt(8)
	v_lshl_or_b32 v188, v99, 16, v98
	v_lshl_or_b32 v189, v101, 16, v100
	s_mov_b64 exec, s[36:37]
	v_lshl_or_b32 v190, v103, 16, v102
	v_lshl_or_b32 v191, v105, 16, v104
	s_mov_b64 exec, -1
	ds_read_u16 v98, v192 offset:6656
	ds_read_u16 v99, v192 offset:6672
	ds_read_u16 v100, v192 offset:6688
	ds_read_u16 v101, v192 offset:6704
	ds_read_u16 v102, v193 offset:1664
	ds_read_u16 v103, v193 offset:1680
	ds_read_u16 v104, v193 offset:1696
	ds_read_u16 v105, v193 offset:1712
	s_waitcnt lgkmcnt(8)
	v_lshl_or_b32 v232, v83, 16, v82
	v_lshl_or_b32 v233, v85, 16, v84
	s_mov_b64 exec, s[36:37]
	v_lshl_or_b32 v234, v91, 16, v90
	v_lshl_or_b32 v235, v93, 16, v92
	s_mov_b64 exec, -1
	ds_read_u16 v82, v192 offset:7168
	ds_read_u16 v83, v192 offset:7184
	ds_read_u16 v84, v192 offset:7200
	ds_read_u16 v85, v192 offset:7216
	ds_read_u16 v90, v193 offset:1792
	ds_read_u16 v91, v193 offset:1808
	ds_read_u16 v92, v193 offset:1824
	ds_read_u16 v93, v193 offset:1840
	s_waitcnt lgkmcnt(8)
	v_lshl_or_b32 v236, v99, 16, v98
	v_lshl_or_b32 v237, v101, 16, v100
	s_mov_b64 exec, s[36:37]
	v_lshl_or_b32 v238, v103, 16, v102
	v_lshl_or_b32 v239, v105, 16, v104
	s_mov_b64 exec, -1
	ds_read_u16 v98, v192 offset:7680
	ds_read_u16 v99, v192 offset:7696
	ds_read_u16 v100, v192 offset:7712
	ds_read_u16 v101, v192 offset:7728
	ds_read_u16 v102, v193 offset:1920
	ds_read_u16 v103, v193 offset:1936
	ds_read_u16 v104, v193 offset:1952
	ds_read_u16 v105, v193 offset:1968
	s_waitcnt lgkmcnt(8)
	v_lshl_or_b32 v240, v83, 16, v82
	v_lshl_or_b32 v241, v85, 16, v84
	s_mov_b64 exec, s[36:37]
	v_lshl_or_b32 v242, v91, 16, v90
	v_lshl_or_b32 v243, v93, 16, v92
	s_mov_b64 exec, -1
	s_waitcnt lgkmcnt(0)
	v_lshl_or_b32 v244, v99, 16, v98
	v_lshl_or_b32 v245, v101, 16, v100
	s_mov_b64 exec, s[36:37]
	v_lshl_or_b32 v246, v103, 16, v102
	v_lshl_or_b32 v247, v105, 16, v104
	s_mov_b64 exec, -1
	s_waitcnt lgkmcnt(0)
	s_mov_b64 exec, s[38:39]
	v_cvt_pk_bf16_f32 v66, v2, v195
	v_cvt_pk_bf16_f32 v74, v3, v195
	v_lshlrev_b32_e32 v67, 16, v66
	v_lshlrev_b32_e32 v75, 16, v74
	v_sub_f32_e32 v2, v2, v67
	v_sub_f32_e32 v3, v3, v75
	v_cvt_pk_bf16_f32 v68, v2, v195
	v_cvt_pk_bf16_f32 v76, v3, v195
	v_lshlrev_b32_e32 v69, 16, v68
	v_lshlrev_b32_e32 v77, 16, v76
	v_sub_f32_e32 v2, v2, v69
	v_sub_f32_e32 v3, v3, v77
	v_cvt_pk_bf16_f32 v147, v2, v195
	v_cvt_pk_bf16_f32 v151, v3, v195
	v_cvt_pk_bf16_f32 v146, v67, v69
	v_cvt_pk_bf16_f32 v150, v75, v77
	v_cvt_pk_bf16_f32 v66, v4, v195
	v_cvt_pk_bf16_f32 v74, v5, v195
	v_lshlrev_b32_e32 v67, 16, v66
	v_lshlrev_b32_e32 v75, 16, v74
	v_sub_f32_e32 v4, v4, v67
	v_sub_f32_e32 v5, v5, v75
	v_cvt_pk_bf16_f32 v68, v4, v195
	v_cvt_pk_bf16_f32 v76, v5, v195
	v_lshlrev_b32_e32 v69, 16, v68
	v_lshlrev_b32_e32 v77, 16, v76
	v_sub_f32_e32 v4, v4, v69
	v_sub_f32_e32 v5, v5, v77
	v_cvt_pk_bf16_f32 v155, v4, v195
	v_cvt_pk_bf16_f32 v159, v5, v195
	v_cvt_pk_bf16_f32 v154, v67, v69
	v_cvt_pk_bf16_f32 v158, v75, v77
	v_cvt_pk_bf16_f32 v66, v6, v195
	v_cvt_pk_bf16_f32 v74, v7, v195
	v_lshlrev_b32_e32 v67, 16, v66
	v_lshlrev_b32_e32 v75, 16, v74
	v_sub_f32_e32 v6, v6, v67
	v_sub_f32_e32 v7, v7, v75
	v_cvt_pk_bf16_f32 v68, v6, v195
	v_cvt_pk_bf16_f32 v76, v7, v195
	v_lshlrev_b32_e32 v69, 16, v68
	v_lshlrev_b32_e32 v77, 16, v76
	v_sub_f32_e32 v6, v6, v69
	v_sub_f32_e32 v7, v7, v77
	v_cvt_pk_bf16_f32 v163, v6, v195
	v_cvt_pk_bf16_f32 v167, v7, v195
	v_cvt_pk_bf16_f32 v162, v67, v69
	v_cvt_pk_bf16_f32 v166, v75, v77
	v_cvt_pk_bf16_f32 v66, v8, v195
	v_cvt_pk_bf16_f32 v74, v9, v195
	v_lshlrev_b32_e32 v67, 16, v66
	v_lshlrev_b32_e32 v75, 16, v74
	v_sub_f32_e32 v8, v8, v67
	v_sub_f32_e32 v9, v9, v75
	v_cvt_pk_bf16_f32 v68, v8, v195
	v_cvt_pk_bf16_f32 v76, v9, v195
	v_lshlrev_b32_e32 v69, 16, v68
	v_lshlrev_b32_e32 v77, 16, v76
	v_sub_f32_e32 v8, v8, v69
	v_sub_f32_e32 v9, v9, v77
	v_cvt_pk_bf16_f32 v171, v8, v195
	v_cvt_pk_bf16_f32 v175, v9, v195
	v_cvt_pk_bf16_f32 v170, v67, v69
	v_cvt_pk_bf16_f32 v174, v75, v77
	v_cvt_pk_bf16_f32 v66, v50, v195
	v_cvt_pk_bf16_f32 v74, v51, v195
	v_lshlrev_b32_e32 v67, 16, v66
	v_lshlrev_b32_e32 v75, 16, v74
	v_sub_f32_e32 v50, v50, v67
	v_sub_f32_e32 v51, v51, v75
	v_cvt_pk_bf16_f32 v68, v50, v195
	v_cvt_pk_bf16_f32 v76, v51, v195
	v_lshlrev_b32_e32 v69, 16, v68
	v_lshlrev_b32_e32 v77, 16, v76
	v_sub_f32_e32 v50, v50, v69
	v_sub_f32_e32 v51, v51, v77
	v_cvt_pk_bf16_f32 v179, v50, v195
	v_cvt_pk_bf16_f32 v183, v51, v195
	v_cvt_pk_bf16_f32 v178, v67, v69
	v_cvt_pk_bf16_f32 v182, v75, v77
	v_cvt_pk_bf16_f32 v66, v52, v195
	v_cvt_pk_bf16_f32 v74, v53, v195
	v_lshlrev_b32_e32 v67, 16, v66
	v_lshlrev_b32_e32 v75, 16, v74
	v_sub_f32_e32 v52, v52, v67
	v_sub_f32_e32 v53, v53, v75
	v_cvt_pk_bf16_f32 v68, v52, v195
	v_cvt_pk_bf16_f32 v76, v53, v195
	v_lshlrev_b32_e32 v69, 16, v68
	v_lshlrev_b32_e32 v77, 16, v76
	v_sub_f32_e32 v52, v52, v69
	v_sub_f32_e32 v53, v53, v77
	v_cvt_pk_bf16_f32 v187, v52, v195
	v_cvt_pk_bf16_f32 v191, v53, v195
	v_cvt_pk_bf16_f32 v186, v67, v69
	v_cvt_pk_bf16_f32 v190, v75, v77
	v_cvt_pk_bf16_f32 v66, v58, v195
	v_cvt_pk_bf16_f32 v74, v59, v195
	v_lshlrev_b32_e32 v67, 16, v66
	v_lshlrev_b32_e32 v75, 16, v74
	v_sub_f32_e32 v58, v58, v67
	v_sub_f32_e32 v59, v59, v75
	v_cvt_pk_bf16_f32 v68, v58, v195
	v_cvt_pk_bf16_f32 v76, v59, v195
	v_lshlrev_b32_e32 v69, 16, v68
	v_lshlrev_b32_e32 v77, 16, v76
	v_sub_f32_e32 v58, v58, v69
	v_sub_f32_e32 v59, v59, v77
	v_cvt_pk_bf16_f32 v235, v58, v195
	v_cvt_pk_bf16_f32 v239, v59, v195
	v_cvt_pk_bf16_f32 v234, v67, v69
	v_cvt_pk_bf16_f32 v238, v75, v77
	v_cvt_pk_bf16_f32 v66, v60, v195
	v_cvt_pk_bf16_f32 v74, v61, v195
	v_lshlrev_b32_e32 v67, 16, v66
	v_lshlrev_b32_e32 v75, 16, v74
	v_sub_f32_e32 v60, v60, v67
	v_sub_f32_e32 v61, v61, v75
	v_cvt_pk_bf16_f32 v68, v60, v195
	v_cvt_pk_bf16_f32 v76, v61, v195
	v_lshlrev_b32_e32 v69, 16, v68
	v_lshlrev_b32_e32 v77, 16, v76
	v_sub_f32_e32 v60, v60, v69
	v_sub_f32_e32 v61, v61, v77
	v_cvt_pk_bf16_f32 v243, v60, v195
	v_cvt_pk_bf16_f32 v247, v61, v195
	v_cvt_pk_bf16_f32 v242, v67, v69
	v_cvt_pk_bf16_f32 v246, v75, v77
	s_mov_b64 exec, -1
	s_movk_i32 s44, 0x210
	v_and_b32_e32 v192, 48, v0
	v_lshrrev_b32_e32 v193, 5, v1
	v_mad_u32_u24 v214, v197, s44, v199
	v_mad_u32_u24 v215, v193, s44, v199
	v_add_u32_e32 v214, v214, v192
	v_and_b32_e32 v192, 0x1f0, v194
	v_add_u32_e32 v215, v215, v192
	s_and_b32 s44, s2, 7
	s_lshl_b32 s44, s44, 22
	s_lshl_b32 s45, s3, 17
	s_add_i32 s44, s44, s45
	v_lshlrev_b32_e32 v220, 13, v193
	v_or3_b32 v220, s44, v220, v196
	v_add_u32_e32 v220, v220, v192
	v_or_b32_e32 v203, 0x24800, v198
	s_mov_b32 s12, 0
	s_mov_b32 s11, 0x20000
	s_brev_b32 s10, 8
	s_and_b32 s9, s9, 0xffff
	v_lshlrev_b32_e32 v192, 3, v142
	v_and_b32_e32 v192, 56, v192
	v_lshl_or_b32 v193, v192, 8, v204
	v_lshl_or_b32 v192, v192, 10, v198
	s_nop 4
	v_mfma_f32_16x16x32_bf16 v[2:5], v[26:29], v[42:45], v[18:21]
	s_nop 1
	ds_read_b128 v[58:61], v192
	ds_read_b128 v[110:113], v193
	ds_read_b128 v[50:53], v192 offset:1024
	ds_read_b128 v[118:121], v193 offset:256
	ds_read_b128 v[66:69], v192 offset:2048
	ds_read_b128 v[126:129], v193 offset:512
	ds_read_b128 v[74:77], v192 offset:3072
	ds_read_b128 v[134:137], v193 offset:768
	ds_read_b128 v[82:85], v192 offset:4096
	ds_read_b128 v[138:141], v193 offset:1024
	ds_read_b128 v[90:93], v192 offset:5120
	ds_read_b128 v[18:21], v193 offset:1280
	ds_read_b128 v[98:101], v192 offset:6144
	ds_read_b128 v[26:29], v193 offset:1536
	ds_read_b128 v[102:105], v192 offset:7168
	ds_read_b128 v[42:45], v193 offset:1792
	s_waitcnt vmcnt(15)
	v_cvt_pk_bf16_f32 v6, v10, v11
	v_cvt_pk_bf16_f32 v7, v12, v13
	ds_write_b64 v212, v[6:7]
	s_waitcnt vmcnt(14)
	v_cvt_pk_bf16_f32 v6, v14, v15
	v_cvt_pk_bf16_f32 v7, v16, v17
	ds_write_b64 v211, v[6:7] offset:512
	s_waitcnt vmcnt(13)
	v_cvt_pk_bf16_f32 v6, v22, v23
	v_cvt_pk_bf16_f32 v7, v24, v25
	ds_write_b64 v210, v[6:7] offset:1024
	s_waitcnt vmcnt(12)
	v_cvt_pk_bf16_f32 v6, v30, v31
	v_cvt_pk_bf16_f32 v7, v32, v33
	ds_write_b64 v209, v[6:7] offset:1536
	s_waitcnt vmcnt(11)
	v_cvt_pk_bf16_f32 v6, v38, v39
	v_cvt_pk_bf16_f32 v7, v40, v41
	ds_write_b64 v208, v[6:7] offset:2048
	s_waitcnt vmcnt(10)
	v_cvt_pk_bf16_f32 v6, v46, v47
	v_cvt_pk_bf16_f32 v7, v48, v49
	ds_write_b64 v207, v[6:7] offset:2560
	s_waitcnt vmcnt(9)
	v_cvt_pk_bf16_f32 v6, v54, v55
	v_cvt_pk_bf16_f32 v7, v56, v57
	ds_write_b64 v206, v[6:7] offset:3072
	s_waitcnt vmcnt(8)
	v_cvt_pk_bf16_f32 v6, v62, v63
	v_cvt_pk_bf16_f32 v7, v64, v65
	ds_write_b64 v205, v[6:7] offset:3584
	s_waitcnt vmcnt(7)
	v_cvt_pk_bf16_f32 v6, v70, v71
	v_cvt_pk_bf16_f32 v7, v72, v73
	ds_write_b64 v231, v[6:7] offset:4096
	s_waitcnt vmcnt(6)
	v_cvt_pk_bf16_f32 v6, v78, v79
	v_cvt_pk_bf16_f32 v7, v80, v81
	ds_write_b64 v230, v[6:7] offset:4608
	s_waitcnt vmcnt(5)
	v_cvt_pk_bf16_f32 v6, v86, v87
	v_cvt_pk_bf16_f32 v7, v88, v89
	ds_write_b64 v229, v[6:7] offset:5120
	s_waitcnt vmcnt(4)
	v_cvt_pk_bf16_f32 v6, v94, v95
	v_cvt_pk_bf16_f32 v7, v96, v97
	ds_write_b64 v228, v[6:7] offset:5632
	s_waitcnt vmcnt(3)
	v_cvt_pk_bf16_f32 v6, v106, v107
	v_cvt_pk_bf16_f32 v7, v108, v109
	ds_write_b64 v227, v[6:7] offset:6144
	s_waitcnt vmcnt(2)
	v_cvt_pk_bf16_f32 v6, v114, v115
	v_cvt_pk_bf16_f32 v7, v116, v117
	ds_write_b64 v226, v[6:7] offset:6656
	s_waitcnt vmcnt(1)
	v_cvt_pk_bf16_f32 v6, v122, v123
	v_cvt_pk_bf16_f32 v7, v124, v125
	ds_write_b64 v225, v[6:7] offset:7168
	s_waitcnt vmcnt(0)
	v_cvt_pk_bf16_f32 v6, v130, v131
	v_cvt_pk_bf16_f32 v7, v132, v133
	ds_write_b64 v224, v[6:7] offset:7680
	ds_read_b128 v[54:57], v223
	ds_read_b128 v[62:65], v222
	ds_read_b128 v[10:13], v221
	ds_read_b128 v[14:17], v219
	ds_read_b128 v[22:25], v218
	ds_read_b128 v[30:33], v217
	ds_read_b128 v[38:41], v216
	ds_read_b128 v[46:49], v213
	s_waitcnt lgkmcnt(7)
	v_mfma_f32_16x16x32_bf16 v[34:37], v[58:61], v[54:57], v[34:37]
	v_mfma_f32_16x16x32_bf16 v[2:5], v[110:113], v[54:57], v[2:5]
	s_waitcnt lgkmcnt(6)
	v_mfma_f32_16x16x32_bf16 v[34:37], v[50:53], v[62:65], v[34:37]
	v_mfma_f32_16x16x32_bf16 v[2:5], v[118:121], v[62:65], v[2:5]
	s_waitcnt lgkmcnt(5)
	v_mfma_f32_16x16x32_bf16 v[34:37], v[66:69], v[10:13], v[34:37]
	v_mfma_f32_16x16x32_bf16 v[2:5], v[126:129], v[10:13], v[2:5]
	s_waitcnt lgkmcnt(4)
	v_mfma_f32_16x16x32_bf16 v[34:37], v[74:77], v[14:17], v[34:37]
	v_mfma_f32_16x16x32_bf16 v[2:5], v[134:137], v[14:17], v[2:5]
	s_waitcnt lgkmcnt(3)
	v_mfma_f32_16x16x32_bf16 v[34:37], v[82:85], v[22:25], v[34:37]
	v_mfma_f32_16x16x32_bf16 v[2:5], v[138:141], v[22:25], v[2:5]
	s_waitcnt lgkmcnt(2)
	v_mfma_f32_16x16x32_bf16 v[34:37], v[90:93], v[30:33], v[34:37]
	v_mfma_f32_16x16x32_bf16 v[2:5], v[18:21], v[30:33], v[2:5]
	s_waitcnt lgkmcnt(1)
	v_mfma_f32_16x16x32_bf16 v[34:37], v[98:101], v[38:41], v[34:37]
	v_mfma_f32_16x16x32_bf16 v[2:5], v[26:29], v[38:41], v[2:5]
	s_waitcnt lgkmcnt(0)
	v_mfma_f32_16x16x32_bf16 v[56:59], v[102:105], v[46:49], v[34:37]
	v_mfma_f32_16x16x32_bf16 v[60:63], v[42:45], v[46:49], v[2:5]
	v_add_u32_e32 v76, 0x24800, v196
	s_waitcnt lgkmcnt(0)
	v_cmp_gt_u32_e64 s[0:1], 16, v1
	v_cmp_lt_u32_e32 vcc, 15, v1
	s_waitcnt lgkmcnt(0)
	s_nop 2
	v_max_f32_e32 v2, v59, v59
	v_max_f32_e32 v3, v58, v58
	s_waitcnt lgkmcnt(0)
	v_max_f32_e32 v2, v3, v2
	s_nop 0
	s_nop 0
	s_nop 0
	s_waitcnt lgkmcnt(0)
	s_nop 0
	s_nop 0
	s_and_saveexec_b64 s[4:5], vcc
	s_xor_b64 s[4:5], exec, s[4:5]
	s_or_saveexec_b64 s[4:5], s[4:5]
	v_max3_f32 v53, v56, v57, v2
	s_xor_b64 exec, exec, s[4:5]
	v_max_f32_e32 v2, v61, v61
	v_max_f32_e32 v3, v60, v60
	v_max_f32_e32 v2, v3, v2
	v_max_f32_e32 v3, v63, v63
	v_max_f32_e32 v4, v62, v62
	v_max_f32_e32 v3, v4, v3
	v_max3_f32 v53, v53, v2, v3
	s_or_b64 exec, exec, s[4:5]
	v_cmp_eq_u32_e64 s[4:5], 1, v201
	v_max_f32_e32 v53, v53, v53
	v_mov_b32_e32 v68, v53
	s_nop 1
	v_permlane16_swap_b32_e32 v53, v68
	v_max_f32_e32 v68, v53, v68
	v_mov_b32_e32 v55, v68
	s_nop 1
	v_permlane32_swap_b32_e32 v68, v55
	v_max_f32_e32 v68, v68, v55
	v_sub_f32_e32 v55, v56, v68
	v_mul_f32_e32 v55, 0x3fb8aa3b, v55
	v_exp_f32_e32 v70, v55
	v_sub_f32_e32 v55, v57, v68
	v_sub_f32_e32 v57, v59, v68
	v_mul_f32_e32 v57, 0x3fb8aa3b, v57
	v_mul_f32_e32 v55, 0x3fb8aa3b, v55
	v_exp_f32_e32 v59, v57
	v_sub_f32_e32 v57, v60, v68
	v_exp_f32_e32 v71, v55
	v_sub_f32_e32 v55, v58, v68
	v_mul_f32_e32 v57, 0x3fb8aa3b, v57
	v_sub_f32_e32 v58, v61, v68
	v_exp_f32_e32 v57, v57
	v_mul_f32_e32 v58, 0x3fb8aa3b, v58
	v_exp_f32_e32 v58, v58
	v_mul_f32_e32 v55, 0x3fb8aa3b, v55
	v_exp_f32_e32 v72, v55
	v_cndmask_b32_e64 v60, 0, v57, s[0:1]
	v_sub_f32_e32 v57, v62, v68
	v_add_f32_e32 v56, 0, v70
	v_cndmask_b32_e64 v61, 0, v58, s[0:1]
	v_mul_f32_e32 v57, 0x3fb8aa3b, v57
	v_sub_f32_e32 v58, v63, v68
	v_add_f32_e32 v56, v56, v71
	v_exp_f32_e32 v57, v57
	v_mul_f32_e32 v58, 0x3fb8aa3b, v58
	v_add_f32_e32 v56, v56, v72
	v_exp_f32_e32 v58, v58
	v_add_f32_e32 v56, v56, v59
	v_add_f32_e32 v56, v56, v60
	v_add_f32_e32 v56, v56, v61
	v_cndmask_b32_e64 v62, 0, v57, s[0:1]
	v_add_f32_e32 v56, v56, v62
	v_cndmask_b32_e64 v63, 0, v58, s[0:1]
	v_add_f32_e32 v57, v56, v63
	v_mov_b32_e32 v58, v57
	s_nop 1
	v_permlane16_swap_b32_e32 v57, v58
	v_add_f32_e32 v58, v57, v58
	v_mov_b32_e32 v68, v58
	s_nop 1
	v_permlane32_swap_b32_e32 v58, v68
	v_add_f32_e32 v68, v58, v68
	v_div_scale_f32 v69, s[6:7], v68, v68, 1.0
	v_rcp_f32_e32 v73, v69
	s_nop 0
	v_fma_f32 v75, -v69, v73, 1.0
	v_fmac_f32_e32 v73, v75, v73
	v_div_scale_f32 v75, vcc, 1.0, v68, 1.0
	v_mul_f32_e32 v92, v75, v73
	v_fma_f32 v93, -v69, v92, v75
	v_fmac_f32_e32 v92, v93, v73
	v_fma_f32 v69, -v69, v92, v75
	v_div_fmas_f32 v69, v69, v73, v92
	v_div_fixup_f32 v68, v69, v68, 1.0
	v_mov_b32_e32 v73, 0x3b23d70a
	v_mov_b32_e32 v75, 0xf149f2ca
	v_mul_f32_e32 v69, v68, v70
	v_mul_f32_e32 v92, v68, v60
	v_mul_f32_e32 v70, v68, v71
	v_mul_f32_e32 v71, v68, v61
	v_mul_f32_e32 v72, v68, v72
	v_mul_f32_e32 v62, v68, v62
	v_mul_f32_e32 v93, v68, v59
	v_mul_f32_e32 v63, v68, v63
	v_med3_f32 v60, v69, -v73, v73
	v_med3_f32 v61, v92, -v73, v73
	v_med3_f32 v59, v70, -v73, v73
	v_med3_f32 v84, v71, -v73, v73
	v_sub_f32_e32 v69, v69, v60
	v_sub_f32_e32 v92, v92, v61
	v_sub_f32_e32 v70, v70, v59
	v_sub_f32_e32 v71, v71, v84
	v_med3_f32 v60, v72, -v73, v73
	v_med3_f32 v61, v62, -v73, v73
	v_med3_f32 v59, v93, -v73, v73
	v_med3_f32 v84, v63, -v73, v73
	v_sub_f32_e32 v72, v72, v60
	v_sub_f32_e32 v62, v62, v61
	v_sub_f32_e32 v93, v93, v59
	v_sub_f32_e32 v63, v63, v84
	v_max3_f32 v60, v69, v70, v72
	v_max3_f32 v61, v92, v71, v62
	v_max3_f32 v60, v60, v93, v75
	v_max3_f32 v61, v61, v63, v60
	v_cndmask_b32_e64 v60, v60, v61, s[0:1]
	v_mov_b32_e32 v61, v60
	s_nop 1
	v_permlane16_swap_b32_e32 v60, v61
	v_max_f32_e32 v61, v60, v61
	v_mov_b32_e32 v74, v61
	s_nop 1
	v_permlane32_swap_b32_e32 v61, v74
	v_max_f32_e32 v74, v61, v74
	v_sub_f32_e32 v61, v69, v74
	v_mul_f32_e32 v61, 0x3fb8aa3b, v61
	v_exp_f32_e32 v69, v61
	v_sub_f32_e32 v61, v92, v74
	v_mul_f32_e32 v61, 0x3fb8aa3b, v61
	v_exp_f32_e32 v75, v61
	v_sub_f32_e32 v70, v70, v74
	v_sub_f32_e32 v71, v71, v74
	v_mul_f32_e32 v70, 0x3fb8aa3b, v70
	v_mul_f32_e32 v71, 0x3fb8aa3b, v71
	v_exp_f32_e32 v70, v70
	v_exp_f32_e32 v71, v71
	v_sub_f32_e32 v72, v72, v74
	v_sub_f32_e32 v62, v62, v74
	v_mul_f32_e32 v72, 0x3fb8aa3b, v72
	v_mul_f32_e32 v62, 0x3fb8aa3b, v62
	v_add_f32_e32 v73, 0, v69
	v_cndmask_b32_e64 v75, 0, v75, s[0:1]
	v_exp_f32_e32 v72, v72
	v_exp_f32_e32 v62, v62
	v_sub_f32_e32 v84, v93, v74
	v_sub_f32_e32 v63, v63, v74
	v_add_f32_e32 v73, v73, v75
	v_mul_f32_e32 v84, 0x3fb8aa3b, v84
	v_mul_f32_e32 v63, 0x3fb8aa3b, v63
	v_add_f32_e32 v73, v73, v70
	v_cndmask_b32_e64 v71, 0, v71, s[0:1]
	v_exp_f32_e32 v84, v84
	v_exp_f32_e32 v63, v63
	v_add_f32_e32 v73, v73, v71
	v_add_f32_e32 v73, v73, v72
	v_cndmask_b32_e64 v74, 0, v62, s[0:1]
	v_add_f32_e32 v62, v73, v74
	v_add_f32_e32 v62, v62, v84
	v_cndmask_b32_e64 v73, 0, v63, s[0:1]
	v_add_f32_e32 v85, v62, v73
	v_mov_b32_e32 v66, v85
	s_nop 1
	v_permlane16_swap_b32_e32 v85, v66
	v_add_f32_e32 v66, v85, v66
	v_mov_b32_e32 v67, v66
	s_nop 1
	v_permlane32_swap_b32_e32 v66, v67
	v_add_f32_e32 v66, v66, v67
	v_div_scale_f32 v67, s[6:7], v66, v66, 1.0
	v_rcp_f32_e32 v78, v67
	s_nop 0
	v_fma_f32 v68, -v67, v78, 1.0
	v_fmac_f32_e32 v78, v68, v78
	v_div_scale_f32 v68, vcc, 1.0, v66, 1.0
	v_mul_f32_e32 v77, v68, v78
	v_fma_f32 v79, -v67, v77, v68
	v_fmac_f32_e32 v77, v79, v78
	v_fma_f32 v67, -v67, v77, v68
	v_div_fmas_f32 v67, v67, v78, v77
	v_div_fixup_f32 v66, v67, v66, 1.0
	v_mov_b32_e32 v67, 0xbd4ccccd
	v_fmaak_f32 v68, v66, v69, 0xbd4ccccd
	v_fmaak_f32 v69, v66, v70, 0xbd4ccccd
	v_fmaak_f32 v70, v66, v72, 0xbd4ccccd
	v_fmaak_f32 v75, v66, v75, 0xbd4ccccd
	v_fmaak_f32 v71, v66, v71, 0xbd4ccccd
	v_fmaak_f32 v74, v66, v74, 0xbd4ccccd
	v_mul_f32_e32 v70, 0x4038aa3b, v70
	v_fmaak_f32 v72, v66, v84, 0xbd4ccccd
	v_mul_f32_e32 v75, 0x4038aa3b, v75
	v_mul_f32_e32 v71, 0x4038aa3b, v71
	v_mul_f32_e32 v74, 0x4038aa3b, v74
	v_fmac_f32_e32 v67, v66, v73
	v_mul_f32_e32 v68, 0x4038aa3b, v68
	v_mul_f32_e32 v69, 0x4038aa3b, v69
	v_mul_f32_e32 v72, 0x4038aa3b, v72
	v_cndmask_b32_e64 v75, 0, v75, s[0:1]
	v_cndmask_b32_e64 v71, 0, v71, s[0:1]
	v_cndmask_b32_e64 v74, 0, v74, s[0:1]
	v_mul_f32_e32 v66, 0x4038aa3b, v67
	v_cvt_pk_bf16_f32 v67, v70, v72
	v_add_u32_e32 v70, v76, v198
	v_cndmask_b32_e64 v73, 0, v66, s[0:1]
	v_cndmask_b32_e64 v74, v74, 1.0, s[4:5]
	v_cndmask_b32_e64 v75, v75, 1.0, s[4:5]
	v_cndmask_b32_e64 v71, v71, 1.0, s[4:5]
	v_cvt_pk_bf16_f32 v66, v68, v69
	v_cvt_pk_bf16_f32 v68, v75, v71
	v_cvt_pk_bf16_f32 v69, v74, v73
	ds_write_b128 v70, v[66:69]
	s_waitcnt lgkmcnt(0)
	s_barrier
